# S1 + snake MFMA issue order (one operand register changes per issue)
# speedup vs baseline: 1.0033x; 1.0015x over previous
.LBB0_478:
	s_cmp_gt_u32 s92, 13
	s_cselect_b64 s[80:81], -1, 0
	s_and_b64 vcc, s[80:81], exec
	s_cselect_b32 s0, -14, 2
	s_add_i32 s80, s0, s92
	s_ashr_i32 s81, s80, 31
	s_lshl_b64 s[80:81], s[80:81], 7
	s_add_u32 s0, s76, s80
	s_addc_u32 s1, s77, s81
	s_add_u32 s82, s42, s80
	s_addc_u32 s83, s43, s81
	s_cmp_gt_u32 s92, 12
	s_cselect_b32 s80, -13, 3
	s_add_i32 s80, s80, s92
	s_ashr_i32 s81, s80, 31
	s_lshl_b64 s[80:81], s[80:81], 7
	s_add_u32 s94, s76, s80
	s_addc_u32 s50, s77, s81
	s_add_u32 s16, s42, s80
	s_addc_u32 s17, s43, s81
	s_cmp_eq_u32 s92, 14
	s_cselect_b32 s84, s70, s0
	s_mov_b32 s0, s92
	v_add_u32_e32 v140, 0x10000, v173
	v_add_u32_e32 v156, 0x14000, v173
	ds_read_b128 v[128:131], v140
	ds_read_b128 v[132:135], v140 offset:1024
	ds_read_b128 v[136:139], v140 offset:2048
	ds_read_b128 v[140:143], v140 offset:3072
	ds_read_b128 v[144:147], v156
	ds_read_b128 v[148:151], v156 offset:1024
	ds_read_b128 v[152:155], v156 offset:2048
	ds_read_b128 v[166:169], v156 offset:3072
	s_cselect_b32 s85, s63, s1
	s_cselect_b32 s87, s72, s83
	s_cselect_b32 s86, s75, s82
	s_cselect_b32 s81, s10, s50
	s_cselect_b32 s80, s9, s94
	s_cselect_b32 s83, s12, s17
	s_cselect_b32 s82, s11, s16
	ds_read_b128 v[176:179], v174
	ds_read_b128 v[180:183], v174 offset:1024
	ds_read_b128 v[184:187], v174 offset:2048
	ds_read_b128 v[190:193], v174 offset:3072
	ds_read_b128 v[194:197], v174 offset:4096
	ds_read_b128 v[198:201], v174 offset:5120
	ds_read_b128 v[202:205], v174 offset:6144
	ds_read_b128 v[206:209], v174 offset:7168
	s_add_u32 s0, s78, 0x40080
	s_addc_u32 s1, s79, 0
	s_mov_b32 m0, s89
	s_nop 0
	global_load_lds_dwordx4 v165, s[0:1]
	s_add_i32 s16, s19, 0xe000
	s_mov_b32 m0, s16
	s_nop 0
	global_load_lds_dwordx4 v171, s[0:1]
	s_setprio 1
	s_waitcnt vmcnt(8)
	s_waitcnt lgkmcnt(0)
	s_barrier
	v_mfma_i32_16x16x64_i8 v[124:127], v[128:131], v[176:179], v[124:127]
	v_mfma_i32_16x16x64_i8 v[120:123], v[136:139], v[176:179], v[120:123]
	v_mfma_i32_16x16x64_i8 v[108:111], v[136:139], v[184:187], v[108:111]
	v_mfma_i32_16x16x64_i8 v[116:119], v[128:131], v[184:187], v[116:119]
	v_mfma_i32_16x16x64_i8 v[100:103], v[128:131], v[194:197], v[100:103]
	v_mfma_i32_16x16x64_i8 v[92:95], v[136:139], v[194:197], v[92:95]
	v_mfma_i32_16x16x64_i8 v[76:79], v[136:139], v[202:205], v[76:79]
	v_mfma_i32_16x16x64_i8 v[84:87], v[128:131], v[202:205], v[84:87]
	v_mfma_i32_16x16x64_i8 v[124:127], v[132:135], v[180:183], v[124:127]
	v_mfma_i32_16x16x64_i8 v[120:123], v[140:143], v[180:183], v[120:123]
	v_mfma_i32_16x16x64_i8 v[108:111], v[140:143], v[190:193], v[108:111]
	v_mfma_i32_16x16x64_i8 v[116:119], v[132:135], v[190:193], v[116:119]
	v_mfma_i32_16x16x64_i8 v[100:103], v[132:135], v[198:201], v[100:103]
	v_mfma_i32_16x16x64_i8 v[92:95], v[140:143], v[198:201], v[92:95]
	v_mfma_i32_16x16x64_i8 v[76:79], v[140:143], v[206:209], v[76:79]
	v_mfma_i32_16x16x64_i8 v[84:87], v[132:135], v[206:209], v[84:87]
	v_mfma_i32_16x16x64_i8 v[112:115], v[144:147], v[176:179], v[112:115]
	v_mfma_i32_16x16x64_i8 v[104:107], v[152:155], v[176:179], v[104:107]
	v_mfma_i32_16x16x64_i8 v[88:91], v[152:155], v[184:187], v[88:91]
	v_mfma_i32_16x16x64_i8 v[96:99], v[144:147], v[184:187], v[96:99]
	v_mfma_i32_16x16x64_i8 v[80:83], v[144:147], v[194:197], v[80:83]
	v_mfma_i32_16x16x64_i8 v[72:75], v[152:155], v[194:197], v[72:75]
	v_mfma_i32_16x16x64_i8 v[64:67], v[152:155], v[202:205], v[64:67]
	v_mfma_i32_16x16x64_i8 v[68:71], v[144:147], v[202:205], v[68:71]
	v_mfma_i32_16x16x64_i8 v[112:115], v[148:151], v[180:183], v[112:115]
	v_mfma_i32_16x16x64_i8 v[104:107], v[166:169], v[180:183], v[104:107]
	v_mfma_i32_16x16x64_i8 v[88:91], v[166:169], v[190:193], v[88:91]
	v_mfma_i32_16x16x64_i8 v[96:99], v[148:151], v[190:193], v[96:99]
	v_mfma_i32_16x16x64_i8 v[80:83], v[148:151], v[198:201], v[80:83]
	v_mfma_i32_16x16x64_i8 v[72:75], v[166:169], v[198:201], v[72:75]
	v_mfma_i32_16x16x64_i8 v[64:67], v[166:169], v[206:209], v[64:67]
	v_mfma_i32_16x16x64_i8 v[68:71], v[148:151], v[206:209], v[68:71]
	s_barrier
	s_setprio 0
	ds_read_b128 v[176:179], v174 offset:16384
	ds_read_b128 v[180:183], v174 offset:17408
	ds_read_b128 v[184:187], v174 offset:18432
	ds_read_b128 v[190:193], v174 offset:19456
	ds_read_b128 v[194:197], v174 offset:20480
	ds_read_b128 v[198:201], v174 offset:21504
	ds_read_b128 v[202:205], v174 offset:22528
	ds_read_b128 v[206:209], v174 offset:23552
	s_mov_b32 m0, s27
	s_nop 0
	global_load_lds_dwordx4 v170, s[86:87]
	s_nop 0
	s_mov_b32 m0, s28
	s_nop 0
	global_load_lds_dwordx4 v172, s[86:87]
	s_add_u32 s0, s86, 0x40000
	s_addc_u32 s1, s87, 0
	s_mov_b32 m0, s29
	s_nop 0
	global_load_lds_dwordx4 v170, s[0:1]
	s_nop 0
	s_mov_b32 m0, s34
	s_nop 0
	global_load_lds_dwordx4 v172, s[0:1]
	s_mov_b32 m0, s19
	s_nop 0
	global_load_lds_dwordx4 v165, s[84:85]
	s_nop 0
	s_mov_b32 m0, s35
	s_nop 0
	global_load_lds_dwordx4 v171, s[84:85]
	s_setprio 1
	s_waitcnt vmcnt(8)
	s_waitcnt lgkmcnt(0)
	s_barrier
	v_mfma_i32_16x16x64_i8 v[60:63], v[128:131], v[176:179], v[60:63]
	v_mfma_i32_16x16x64_i8 v[56:59], v[136:139], v[176:179], v[56:59]
	v_mfma_i32_16x16x64_i8 v[44:47], v[136:139], v[184:187], v[44:47]
	v_mfma_i32_16x16x64_i8 v[52:55], v[128:131], v[184:187], v[52:55]
	v_mfma_i32_16x16x64_i8 v[36:39], v[128:131], v[194:197], v[36:39]
	v_mfma_i32_16x16x64_i8 v[28:31], v[136:139], v[194:197], v[28:31]
	v_mfma_i32_16x16x64_i8 v[12:15], v[136:139], v[202:205], v[12:15]
	v_mfma_i32_16x16x64_i8 v[20:23], v[128:131], v[202:205], v[20:23]
	v_mfma_i32_16x16x64_i8 v[60:63], v[132:135], v[180:183], v[60:63]
	v_mfma_i32_16x16x64_i8 v[56:59], v[140:143], v[180:183], v[56:59]
	v_mfma_i32_16x16x64_i8 v[44:47], v[140:143], v[190:193], v[44:47]
	v_mfma_i32_16x16x64_i8 v[52:55], v[132:135], v[190:193], v[52:55]
	v_mfma_i32_16x16x64_i8 v[36:39], v[132:135], v[198:201], v[36:39]
	v_mfma_i32_16x16x64_i8 v[28:31], v[140:143], v[198:201], v[28:31]
	v_mfma_i32_16x16x64_i8 v[12:15], v[140:143], v[206:209], v[12:15]
	v_mfma_i32_16x16x64_i8 v[20:23], v[132:135], v[206:209], v[20:23]
	v_mfma_i32_16x16x64_i8 v[48:51], v[144:147], v[176:179], v[48:51]
	v_mfma_i32_16x16x64_i8 v[40:43], v[152:155], v[176:179], v[40:43]
	v_mfma_i32_16x16x64_i8 v[24:27], v[152:155], v[184:187], v[24:27]
	v_mfma_i32_16x16x64_i8 v[32:35], v[144:147], v[184:187], v[32:35]
	v_mfma_i32_16x16x64_i8 v[16:19], v[144:147], v[194:197], v[16:19]
	v_mfma_i32_16x16x64_i8 v[8:11], v[152:155], v[194:197], v[8:11]
	v_mfma_i32_16x16x64_i8 v[0:3], v[152:155], v[202:205], v[0:3]
	v_mfma_i32_16x16x64_i8 v[4:7], v[144:147], v[202:205], v[4:7]
	v_mfma_i32_16x16x64_i8 v[48:51], v[148:151], v[180:183], v[48:51]
	v_mfma_i32_16x16x64_i8 v[40:43], v[166:169], v[180:183], v[40:43]
	v_mfma_i32_16x16x64_i8 v[24:27], v[166:169], v[190:193], v[24:27]
	v_mfma_i32_16x16x64_i8 v[32:35], v[148:151], v[190:193], v[32:35]
	v_mfma_i32_16x16x64_i8 v[16:19], v[148:151], v[198:201], v[16:19]
	v_mfma_i32_16x16x64_i8 v[8:11], v[166:169], v[198:201], v[8:11]
	v_mfma_i32_16x16x64_i8 v[0:3], v[166:169], v[206:209], v[0:3]
	v_mfma_i32_16x16x64_i8 v[4:7], v[148:151], v[206:209], v[4:7]
	s_barrier
	s_setprio 0
	v_add_u32_e32 v140, 0x18000, v173
	v_add_u32_e32 v156, 0x1c000, v173
	ds_read_b128 v[128:131], v140
	ds_read_b128 v[132:135], v140 offset:1024
	ds_read_b128 v[136:139], v140 offset:2048
	ds_read_b128 v[140:143], v140 offset:3072
	ds_read_b128 v[144:147], v156
	ds_read_b128 v[148:151], v156 offset:1024
	ds_read_b128 v[152:155], v156 offset:2048
	ds_read_b128 v[166:169], v156 offset:3072
	ds_read_b128 v[176:179], v174 offset:32768
	ds_read_b128 v[180:183], v174 offset:33792
	ds_read_b128 v[184:187], v174 offset:34816
	ds_read_b128 v[190:193], v174 offset:35840
	ds_read_b128 v[194:197], v174 offset:36864
	ds_read_b128 v[198:201], v174 offset:37888
	ds_read_b128 v[202:205], v174 offset:38912
	ds_read_b128 v[206:209], v174 offset:39936
	s_add_u32 s0, s84, 0x40000
	s_addc_u32 s1, s85, 0
	s_mov_b32 m0, s36
	s_nop 0
	global_load_lds_dwordx4 v165, s[0:1]
	s_nop 0
	s_mov_b32 m0, s37
	s_nop 0
	global_load_lds_dwordx4 v171, s[0:1]
	s_setprio 1
	s_waitcnt vmcnt(8)
	s_waitcnt lgkmcnt(0)
	s_barrier
	v_mfma_i32_16x16x64_i8 v[124:127], v[128:131], v[176:179], v[124:127]
	v_mfma_i32_16x16x64_i8 v[120:123], v[136:139], v[176:179], v[120:123]
	v_mfma_i32_16x16x64_i8 v[108:111], v[136:139], v[184:187], v[108:111]
	v_mfma_i32_16x16x64_i8 v[116:119], v[128:131], v[184:187], v[116:119]
	v_mfma_i32_16x16x64_i8 v[100:103], v[128:131], v[194:197], v[100:103]
	v_mfma_i32_16x16x64_i8 v[92:95], v[136:139], v[194:197], v[92:95]
	v_mfma_i32_16x16x64_i8 v[76:79], v[136:139], v[202:205], v[76:79]
	v_mfma_i32_16x16x64_i8 v[84:87], v[128:131], v[202:205], v[84:87]
	v_mfma_i32_16x16x64_i8 v[124:127], v[132:135], v[180:183], v[124:127]
	v_mfma_i32_16x16x64_i8 v[120:123], v[140:143], v[180:183], v[120:123]
	v_mfma_i32_16x16x64_i8 v[108:111], v[140:143], v[190:193], v[108:111]
	v_mfma_i32_16x16x64_i8 v[116:119], v[132:135], v[190:193], v[116:119]
	v_mfma_i32_16x16x64_i8 v[100:103], v[132:135], v[198:201], v[100:103]
	v_mfma_i32_16x16x64_i8 v[92:95], v[140:143], v[198:201], v[92:95]
	v_mfma_i32_16x16x64_i8 v[76:79], v[140:143], v[206:209], v[76:79]
	v_mfma_i32_16x16x64_i8 v[84:87], v[132:135], v[206:209], v[84:87]
	v_mfma_i32_16x16x64_i8 v[112:115], v[144:147], v[176:179], v[112:115]
	v_mfma_i32_16x16x64_i8 v[104:107], v[152:155], v[176:179], v[104:107]
	v_mfma_i32_16x16x64_i8 v[88:91], v[152:155], v[184:187], v[88:91]
	v_mfma_i32_16x16x64_i8 v[96:99], v[144:147], v[184:187], v[96:99]
	v_mfma_i32_16x16x64_i8 v[80:83], v[144:147], v[194:197], v[80:83]
	v_mfma_i32_16x16x64_i8 v[72:75], v[152:155], v[194:197], v[72:75]
	v_mfma_i32_16x16x64_i8 v[64:67], v[152:155], v[202:205], v[64:67]
	v_mfma_i32_16x16x64_i8 v[68:71], v[144:147], v[202:205], v[68:71]
	v_mfma_i32_16x16x64_i8 v[112:115], v[148:151], v[180:183], v[112:115]
	v_mfma_i32_16x16x64_i8 v[104:107], v[166:169], v[180:183], v[104:107]
	v_mfma_i32_16x16x64_i8 v[88:91], v[166:169], v[190:193], v[88:91]
	v_mfma_i32_16x16x64_i8 v[96:99], v[148:151], v[190:193], v[96:99]
	v_mfma_i32_16x16x64_i8 v[80:83], v[148:151], v[198:201], v[80:83]
	v_mfma_i32_16x16x64_i8 v[72:75], v[166:169], v[198:201], v[72:75]
	v_mfma_i32_16x16x64_i8 v[64:67], v[166:169], v[206:209], v[64:67]
	v_mfma_i32_16x16x64_i8 v[68:71], v[148:151], v[206:209], v[68:71]
	s_barrier
	s_setprio 0
	ds_read_b128 v[176:179], v174 offset:49152
	ds_read_b128 v[180:183], v174 offset:50176
	ds_read_b128 v[184:187], v174 offset:51200
	ds_read_b128 v[190:193], v174 offset:52224
	ds_read_b128 v[194:197], v174 offset:53248
	ds_read_b128 v[198:201], v174 offset:54272
	ds_read_b128 v[202:205], v174 offset:55296
	ds_read_b128 v[206:209], v174 offset:56320
	s_mov_b32 m0, s66
	s_nop 0
	global_load_lds_dwordx4 v170, s[82:83]
	s_nop 0
	s_mov_b32 m0, s67
	s_nop 0
	global_load_lds_dwordx4 v172, s[82:83]
	s_add_u32 s0, s82, 0x40000
	s_addc_u32 s1, s83, 0
	s_mov_b32 m0, s71
	s_nop 0
	global_load_lds_dwordx4 v170, s[0:1]
	s_nop 0
	s_mov_b32 m0, s88
	s_nop 0
	global_load_lds_dwordx4 v172, s[0:1]
	s_mov_b32 m0, s68
	s_nop 0
	global_load_lds_dwordx4 v165, s[80:81]
	s_nop 0
	s_mov_b32 m0, s69
	s_nop 0
	global_load_lds_dwordx4 v171, s[80:81]
	s_setprio 1
	s_waitcnt vmcnt(8)
	s_waitcnt lgkmcnt(0)
	s_barrier
	v_mfma_i32_16x16x64_i8 v[60:63], v[128:131], v[176:179], v[60:63]
	v_mfma_i32_16x16x64_i8 v[56:59], v[136:139], v[176:179], v[56:59]
	v_mfma_i32_16x16x64_i8 v[44:47], v[136:139], v[184:187], v[44:47]
	v_mfma_i32_16x16x64_i8 v[52:55], v[128:131], v[184:187], v[52:55]
	v_mfma_i32_16x16x64_i8 v[36:39], v[128:131], v[194:197], v[36:39]
	v_mfma_i32_16x16x64_i8 v[28:31], v[136:139], v[194:197], v[28:31]
	v_mfma_i32_16x16x64_i8 v[12:15], v[136:139], v[202:205], v[12:15]
	v_mfma_i32_16x16x64_i8 v[20:23], v[128:131], v[202:205], v[20:23]
	v_mfma_i32_16x16x64_i8 v[60:63], v[132:135], v[180:183], v[60:63]
	v_mfma_i32_16x16x64_i8 v[56:59], v[140:143], v[180:183], v[56:59]
	v_mfma_i32_16x16x64_i8 v[44:47], v[140:143], v[190:193], v[44:47]
	v_mfma_i32_16x16x64_i8 v[52:55], v[132:135], v[190:193], v[52:55]
	v_mfma_i32_16x16x64_i8 v[36:39], v[132:135], v[198:201], v[36:39]
	v_mfma_i32_16x16x64_i8 v[28:31], v[140:143], v[198:201], v[28:31]
	v_mfma_i32_16x16x64_i8 v[12:15], v[140:143], v[206:209], v[12:15]
	v_mfma_i32_16x16x64_i8 v[20:23], v[132:135], v[206:209], v[20:23]
	v_mfma_i32_16x16x64_i8 v[48:51], v[144:147], v[176:179], v[48:51]
	v_mfma_i32_16x16x64_i8 v[40:43], v[152:155], v[176:179], v[40:43]
	v_mfma_i32_16x16x64_i8 v[24:27], v[152:155], v[184:187], v[24:27]
	v_mfma_i32_16x16x64_i8 v[32:35], v[144:147], v[184:187], v[32:35]
	v_mfma_i32_16x16x64_i8 v[16:19], v[144:147], v[194:197], v[16:19]
	v_mfma_i32_16x16x64_i8 v[8:11], v[152:155], v[194:197], v[8:11]
	v_mfma_i32_16x16x64_i8 v[0:3], v[152:155], v[202:205], v[0:3]
	v_mfma_i32_16x16x64_i8 v[4:7], v[144:147], v[202:205], v[4:7]
	v_mfma_i32_16x16x64_i8 v[48:51], v[148:151], v[180:183], v[48:51]
	v_mfma_i32_16x16x64_i8 v[40:43], v[166:169], v[180:183], v[40:43]
	v_mfma_i32_16x16x64_i8 v[24:27], v[166:169], v[190:193], v[24:27]
	v_mfma_i32_16x16x64_i8 v[32:35], v[148:151], v[190:193], v[32:35]
	v_mfma_i32_16x16x64_i8 v[16:19], v[148:151], v[198:201], v[16:19]
	v_mfma_i32_16x16x64_i8 v[8:11], v[166:169], v[198:201], v[8:11]
	v_mfma_i32_16x16x64_i8 v[0:3], v[166:169], v[206:209], v[0:3]
	v_mfma_i32_16x16x64_i8 v[4:7], v[148:151], v[206:209], v[4:7]
	s_barrier
	s_setprio 0
	s_add_i32 s92, s92, 2
	s_add_u32 s78, s78, 0x100
	s_addc_u32 s79, s79, 0
	s_cbranch_vccz .LBB0_478
	s_and_b64 vcc, exec, s[58:59]
	s_cbranch_vccz .LBB0_481
	s_barrier

.LBB0_816:
	s_cmp_gt_u32 s81, 13
	s_cselect_b64 s[58:59], -1, 0
	s_and_b64 vcc, s[58:59], exec
	s_cselect_b32 s16, -14, 2
	s_add_i32 s58, s16, s81
	s_ashr_i32 s59, s58, 31
	s_lshl_b64 s[58:59], s[58:59], 7
	s_add_u32 s16, s54, s58
	s_addc_u32 s17, s55, s59
	s_add_u32 s50, s52, s58
	s_addc_u32 s51, s53, s59
	s_cmp_gt_u32 s81, 12
	s_cselect_b32 s58, -13, 3
	s_add_i32 s58, s58, s81
	s_ashr_i32 s59, s58, 31
	s_lshl_b64 s[58:59], s[58:59], 7
	s_add_u32 s60, s54, s58
	s_addc_u32 s61, s55, s59
	s_add_u32 s82, s52, s58
	s_addc_u32 s83, s53, s59
	s_cmp_eq_u32 s81, 14
	s_cselect_b32 s62, s11, s16
	s_mov_b32 s16, s81
	v_add_u32_e32 v146, 0x10000, v136
	v_add_u32_e32 v162, 0x14000, v136
	ds_read_b128 v[128:131], v146
	ds_read_b128 v[138:141], v146 offset:1024
	ds_read_b128 v[142:145], v146 offset:2048
	ds_read_b128 v[146:149], v146 offset:3072
	ds_read_b128 v[150:153], v162
	ds_read_b128 v[154:157], v162 offset:1024
	ds_read_b128 v[158:161], v162 offset:2048
	ds_read_b128 v[162:165], v162 offset:3072
	s_cselect_b32 s63, s10, s17
	s_cselect_b32 s75, s12, s51
	s_cselect_b32 s74, s27, s50
	s_cselect_b32 s59, s78, s61
	s_cselect_b32 s58, s45, s60
	s_cselect_b32 s61, s80, s83
	s_cselect_b32 s60, s79, s82
	ds_read_b128 v[166:169], v137
	ds_read_b128 v[170:173], v137 offset:1024
	ds_read_b128 v[174:177], v137 offset:2048
	ds_read_b128 v[178:181], v137 offset:3072
	ds_read_b128 v[182:185], v137 offset:4096
	ds_read_b128 v[190:193], v137 offset:5120
	ds_read_b128 v[194:197], v137 offset:6144
	ds_read_b128 v[198:201], v137 offset:7168
	s_add_u32 s82, s56, 0x40080
	s_addc_u32 s83, s57, 0
	s_mov_b32 m0, s72
	s_nop 0
	global_load_lds_dwordx4 v132, s[82:83]
	s_add_i32 s16, s19, 0xe000
	s_mov_b32 m0, s16
	s_nop 0
	global_load_lds_dwordx4 v134, s[82:83]
	s_setprio 1
	s_waitcnt vmcnt(8)
	s_waitcnt lgkmcnt(0)
	s_barrier
	v_mfma_f32_16x16x32_bf16 v[124:127], v[128:131], v[166:169], v[124:127]
	v_mfma_f32_16x16x32_bf16 v[120:123], v[142:145], v[166:169], v[120:123]
	v_mfma_f32_16x16x32_bf16 v[104:107], v[142:145], v[174:177], v[104:107]
	v_mfma_f32_16x16x32_bf16 v[108:111], v[128:131], v[174:177], v[108:111]
	v_mfma_f32_16x16x32_bf16 v[92:95], v[128:131], v[182:185], v[92:95]
	v_mfma_f32_16x16x32_bf16 v[88:91], v[142:145], v[182:185], v[88:91]
	v_mfma_f32_16x16x32_bf16 v[72:75], v[142:145], v[194:197], v[72:75]
	v_mfma_f32_16x16x32_bf16 v[76:79], v[128:131], v[194:197], v[76:79]
	v_mfma_f32_16x16x32_bf16 v[124:127], v[138:141], v[170:173], v[124:127]
	v_mfma_f32_16x16x32_bf16 v[120:123], v[146:149], v[170:173], v[120:123]
	v_mfma_f32_16x16x32_bf16 v[104:107], v[146:149], v[178:181], v[104:107]
	v_mfma_f32_16x16x32_bf16 v[108:111], v[138:141], v[178:181], v[108:111]
	v_mfma_f32_16x16x32_bf16 v[92:95], v[138:141], v[190:193], v[92:95]
	v_mfma_f32_16x16x32_bf16 v[88:91], v[146:149], v[190:193], v[88:91]
	v_mfma_f32_16x16x32_bf16 v[72:75], v[146:149], v[198:201], v[72:75]
	v_mfma_f32_16x16x32_bf16 v[76:79], v[138:141], v[198:201], v[76:79]
	v_mfma_f32_16x16x32_bf16 v[116:119], v[150:153], v[166:169], v[116:119]
	v_mfma_f32_16x16x32_bf16 v[112:115], v[158:161], v[166:169], v[112:115]
	v_mfma_f32_16x16x32_bf16 v[96:99], v[158:161], v[174:177], v[96:99]
	v_mfma_f32_16x16x32_bf16 v[100:103], v[150:153], v[174:177], v[100:103]
	v_mfma_f32_16x16x32_bf16 v[84:87], v[150:153], v[182:185], v[84:87]
	v_mfma_f32_16x16x32_bf16 v[80:83], v[158:161], v[182:185], v[80:83]
	v_mfma_f32_16x16x32_bf16 v[64:67], v[158:161], v[194:197], v[64:67]
	v_mfma_f32_16x16x32_bf16 v[68:71], v[150:153], v[194:197], v[68:71]
	v_mfma_f32_16x16x32_bf16 v[116:119], v[154:157], v[170:173], v[116:119]
	v_mfma_f32_16x16x32_bf16 v[112:115], v[162:165], v[170:173], v[112:115]
	v_mfma_f32_16x16x32_bf16 v[96:99], v[162:165], v[178:181], v[96:99]
	v_mfma_f32_16x16x32_bf16 v[100:103], v[154:157], v[178:181], v[100:103]
	v_mfma_f32_16x16x32_bf16 v[84:87], v[154:157], v[190:193], v[84:87]
	v_mfma_f32_16x16x32_bf16 v[80:83], v[162:165], v[190:193], v[80:83]
	v_mfma_f32_16x16x32_bf16 v[64:67], v[162:165], v[198:201], v[64:67]
	v_mfma_f32_16x16x32_bf16 v[68:71], v[154:157], v[198:201], v[68:71]
	s_barrier
	s_setprio 0
	ds_read_b128 v[166:169], v137 offset:16384
	ds_read_b128 v[170:173], v137 offset:17408
	ds_read_b128 v[174:177], v137 offset:18432
	ds_read_b128 v[178:181], v137 offset:19456
	ds_read_b128 v[182:185], v137 offset:20480
	ds_read_b128 v[190:193], v137 offset:21504
	ds_read_b128 v[194:197], v137 offset:22528
	ds_read_b128 v[198:201], v137 offset:23552
	s_mov_b32 m0, s28
	s_nop 0
	global_load_lds_dwordx4 v133, s[74:75]
	s_nop 0
	s_mov_b32 m0, s29
	s_nop 0
	global_load_lds_dwordx4 v135, s[74:75]
	s_add_u32 s74, s74, 0x40000
	s_addc_u32 s75, s75, 0
	s_mov_b32 m0, s30
	s_nop 0
	global_load_lds_dwordx4 v133, s[74:75]
	s_nop 0
	s_mov_b32 m0, s31
	s_nop 0
	global_load_lds_dwordx4 v135, s[74:75]
	s_nop 0
	s_mov_b32 m0, s19
	s_nop 0
	global_load_lds_dwordx4 v132, s[62:63]
	s_nop 0
	s_mov_b32 m0, s34
	s_nop 0
	global_load_lds_dwordx4 v134, s[62:63]
	s_setprio 1
	s_waitcnt vmcnt(8)
	s_waitcnt lgkmcnt(0)
	s_barrier
	v_mfma_f32_16x16x32_bf16 v[60:63], v[128:131], v[166:169], v[60:63]
	v_mfma_f32_16x16x32_bf16 v[56:59], v[142:145], v[166:169], v[56:59]
	v_mfma_f32_16x16x32_bf16 v[40:43], v[142:145], v[174:177], v[40:43]
	v_mfma_f32_16x16x32_bf16 v[44:47], v[128:131], v[174:177], v[44:47]
	v_mfma_f32_16x16x32_bf16 v[28:31], v[128:131], v[182:185], v[28:31]
	v_mfma_f32_16x16x32_bf16 v[24:27], v[142:145], v[182:185], v[24:27]
	v_mfma_f32_16x16x32_bf16 v[8:11], v[142:145], v[194:197], v[8:11]
	v_mfma_f32_16x16x32_bf16 v[12:15], v[128:131], v[194:197], v[12:15]
	v_mfma_f32_16x16x32_bf16 v[60:63], v[138:141], v[170:173], v[60:63]
	v_mfma_f32_16x16x32_bf16 v[56:59], v[146:149], v[170:173], v[56:59]
	v_mfma_f32_16x16x32_bf16 v[40:43], v[146:149], v[178:181], v[40:43]
	v_mfma_f32_16x16x32_bf16 v[44:47], v[138:141], v[178:181], v[44:47]
	v_mfma_f32_16x16x32_bf16 v[28:31], v[138:141], v[190:193], v[28:31]
	v_mfma_f32_16x16x32_bf16 v[24:27], v[146:149], v[190:193], v[24:27]
	v_mfma_f32_16x16x32_bf16 v[8:11], v[146:149], v[198:201], v[8:11]
	v_mfma_f32_16x16x32_bf16 v[12:15], v[138:141], v[198:201], v[12:15]
	v_mfma_f32_16x16x32_bf16 v[52:55], v[150:153], v[166:169], v[52:55]
	v_mfma_f32_16x16x32_bf16 v[48:51], v[158:161], v[166:169], v[48:51]
	v_mfma_f32_16x16x32_bf16 v[32:35], v[158:161], v[174:177], v[32:35]
	v_mfma_f32_16x16x32_bf16 v[36:39], v[150:153], v[174:177], v[36:39]
	v_mfma_f32_16x16x32_bf16 v[20:23], v[150:153], v[182:185], v[20:23]
	v_mfma_f32_16x16x32_bf16 v[16:19], v[158:161], v[182:185], v[16:19]
	v_mfma_f32_16x16x32_bf16 v[0:3], v[158:161], v[194:197], v[0:3]
	v_mfma_f32_16x16x32_bf16 v[4:7], v[150:153], v[194:197], v[4:7]
	v_mfma_f32_16x16x32_bf16 v[52:55], v[154:157], v[170:173], v[52:55]
	v_mfma_f32_16x16x32_bf16 v[48:51], v[162:165], v[170:173], v[48:51]
	v_mfma_f32_16x16x32_bf16 v[32:35], v[162:165], v[178:181], v[32:35]
	v_mfma_f32_16x16x32_bf16 v[36:39], v[154:157], v[178:181], v[36:39]
	v_mfma_f32_16x16x32_bf16 v[20:23], v[154:157], v[190:193], v[20:23]
	v_mfma_f32_16x16x32_bf16 v[16:19], v[162:165], v[190:193], v[16:19]
	v_mfma_f32_16x16x32_bf16 v[0:3], v[162:165], v[198:201], v[0:3]
	v_mfma_f32_16x16x32_bf16 v[4:7], v[154:157], v[198:201], v[4:7]
	s_barrier
	s_setprio 0
	v_add_u32_e32 v146, 0x18000, v136
	v_add_u32_e32 v162, 0x1c000, v136
	ds_read_b128 v[128:131], v146
	ds_read_b128 v[138:141], v146 offset:1024
	ds_read_b128 v[142:145], v146 offset:2048
	ds_read_b128 v[146:149], v146 offset:3072
	ds_read_b128 v[150:153], v162
	ds_read_b128 v[154:157], v162 offset:1024
	ds_read_b128 v[158:161], v162 offset:2048
	ds_read_b128 v[162:165], v162 offset:3072
	ds_read_b128 v[166:169], v137 offset:32768
	ds_read_b128 v[170:173], v137 offset:33792
	ds_read_b128 v[174:177], v137 offset:34816
	ds_read_b128 v[178:181], v137 offset:35840
	ds_read_b128 v[182:185], v137 offset:36864
	ds_read_b128 v[190:193], v137 offset:37888
	ds_read_b128 v[194:197], v137 offset:38912
	ds_read_b128 v[198:201], v137 offset:39936
	s_add_u32 s62, s62, 0x40000
	s_addc_u32 s63, s63, 0
	s_mov_b32 m0, s35
	s_nop 0
	global_load_lds_dwordx4 v132, s[62:63]
	s_nop 0
	s_mov_b32 m0, s36
	s_nop 0
	global_load_lds_dwordx4 v134, s[62:63]
	s_setprio 1
	s_waitcnt vmcnt(8)
	s_waitcnt lgkmcnt(0)
	s_barrier
	v_mfma_f32_16x16x32_bf16 v[124:127], v[128:131], v[166:169], v[124:127]
	v_mfma_f32_16x16x32_bf16 v[120:123], v[142:145], v[166:169], v[120:123]
	v_mfma_f32_16x16x32_bf16 v[104:107], v[142:145], v[174:177], v[104:107]
	v_mfma_f32_16x16x32_bf16 v[108:111], v[128:131], v[174:177], v[108:111]
	v_mfma_f32_16x16x32_bf16 v[92:95], v[128:131], v[182:185], v[92:95]
	v_mfma_f32_16x16x32_bf16 v[88:91], v[142:145], v[182:185], v[88:91]
	v_mfma_f32_16x16x32_bf16 v[72:75], v[142:145], v[194:197], v[72:75]
	v_mfma_f32_16x16x32_bf16 v[76:79], v[128:131], v[194:197], v[76:79]
	v_mfma_f32_16x16x32_bf16 v[124:127], v[138:141], v[170:173], v[124:127]
	v_mfma_f32_16x16x32_bf16 v[120:123], v[146:149], v[170:173], v[120:123]
	v_mfma_f32_16x16x32_bf16 v[104:107], v[146:149], v[178:181], v[104:107]
	v_mfma_f32_16x16x32_bf16 v[108:111], v[138:141], v[178:181], v[108:111]
	v_mfma_f32_16x16x32_bf16 v[92:95], v[138:141], v[190:193], v[92:95]
	v_mfma_f32_16x16x32_bf16 v[88:91], v[146:149], v[190:193], v[88:91]
	v_mfma_f32_16x16x32_bf16 v[72:75], v[146:149], v[198:201], v[72:75]
	v_mfma_f32_16x16x32_bf16 v[76:79], v[138:141], v[198:201], v[76:79]
	v_mfma_f32_16x16x32_bf16 v[116:119], v[150:153], v[166:169], v[116:119]
	v_mfma_f32_16x16x32_bf16 v[112:115], v[158:161], v[166:169], v[112:115]
	v_mfma_f32_16x16x32_bf16 v[96:99], v[158:161], v[174:177], v[96:99]
	v_mfma_f32_16x16x32_bf16 v[100:103], v[150:153], v[174:177], v[100:103]
	v_mfma_f32_16x16x32_bf16 v[84:87], v[150:153], v[182:185], v[84:87]
	v_mfma_f32_16x16x32_bf16 v[80:83], v[158:161], v[182:185], v[80:83]
	v_mfma_f32_16x16x32_bf16 v[64:67], v[158:161], v[194:197], v[64:67]
	v_mfma_f32_16x16x32_bf16 v[68:71], v[150:153], v[194:197], v[68:71]
	v_mfma_f32_16x16x32_bf16 v[116:119], v[154:157], v[170:173], v[116:119]
	v_mfma_f32_16x16x32_bf16 v[112:115], v[162:165], v[170:173], v[112:115]
	v_mfma_f32_16x16x32_bf16 v[96:99], v[162:165], v[178:181], v[96:99]
	v_mfma_f32_16x16x32_bf16 v[100:103], v[154:157], v[178:181], v[100:103]
	v_mfma_f32_16x16x32_bf16 v[84:87], v[154:157], v[190:193], v[84:87]
	v_mfma_f32_16x16x32_bf16 v[80:83], v[162:165], v[190:193], v[80:83]
	v_mfma_f32_16x16x32_bf16 v[64:67], v[162:165], v[198:201], v[64:67]
	v_mfma_f32_16x16x32_bf16 v[68:71], v[154:157], v[198:201], v[68:71]
	s_barrier
	s_setprio 0
	ds_read_b128 v[166:169], v137 offset:49152
	ds_read_b128 v[170:173], v137 offset:50176
	ds_read_b128 v[174:177], v137 offset:51200
	ds_read_b128 v[178:181], v137 offset:52224
	ds_read_b128 v[182:185], v137 offset:53248
	ds_read_b128 v[190:193], v137 offset:54272
	ds_read_b128 v[194:197], v137 offset:55296
	ds_read_b128 v[198:201], v137 offset:56320
	s_mov_b32 m0, s66
	s_nop 0
	global_load_lds_dwordx4 v133, s[60:61]
	s_nop 0
	s_mov_b32 m0, s67
	s_nop 0
	global_load_lds_dwordx4 v135, s[60:61]
	s_add_u32 s60, s60, 0x40000
	s_addc_u32 s61, s61, 0
	s_mov_b32 m0, s70
	s_nop 0
	global_load_lds_dwordx4 v133, s[60:61]
	s_nop 0
	s_mov_b32 m0, s71
	s_nop 0
	global_load_lds_dwordx4 v135, s[60:61]
	s_nop 0
	s_mov_b32 m0, s68
	s_nop 0
	global_load_lds_dwordx4 v132, s[58:59]
	s_nop 0
	s_mov_b32 m0, s69
	s_nop 0
	global_load_lds_dwordx4 v134, s[58:59]
	s_setprio 1
	s_waitcnt vmcnt(8)
	s_waitcnt lgkmcnt(0)
	s_barrier
	v_mfma_f32_16x16x32_bf16 v[60:63], v[128:131], v[166:169], v[60:63]
	v_mfma_f32_16x16x32_bf16 v[56:59], v[142:145], v[166:169], v[56:59]
	v_mfma_f32_16x16x32_bf16 v[40:43], v[142:145], v[174:177], v[40:43]
	v_mfma_f32_16x16x32_bf16 v[44:47], v[128:131], v[174:177], v[44:47]
	v_mfma_f32_16x16x32_bf16 v[28:31], v[128:131], v[182:185], v[28:31]
	v_mfma_f32_16x16x32_bf16 v[24:27], v[142:145], v[182:185], v[24:27]
	v_mfma_f32_16x16x32_bf16 v[8:11], v[142:145], v[194:197], v[8:11]
	v_mfma_f32_16x16x32_bf16 v[12:15], v[128:131], v[194:197], v[12:15]
	v_mfma_f32_16x16x32_bf16 v[60:63], v[138:141], v[170:173], v[60:63]
	v_mfma_f32_16x16x32_bf16 v[56:59], v[146:149], v[170:173], v[56:59]
	v_mfma_f32_16x16x32_bf16 v[40:43], v[146:149], v[178:181], v[40:43]
	v_mfma_f32_16x16x32_bf16 v[44:47], v[138:141], v[178:181], v[44:47]
	v_mfma_f32_16x16x32_bf16 v[28:31], v[138:141], v[190:193], v[28:31]
	v_mfma_f32_16x16x32_bf16 v[24:27], v[146:149], v[190:193], v[24:27]
	v_mfma_f32_16x16x32_bf16 v[8:11], v[146:149], v[198:201], v[8:11]
	v_mfma_f32_16x16x32_bf16 v[12:15], v[138:141], v[198:201], v[12:15]
	v_mfma_f32_16x16x32_bf16 v[52:55], v[150:153], v[166:169], v[52:55]
	v_mfma_f32_16x16x32_bf16 v[48:51], v[158:161], v[166:169], v[48:51]
	v_mfma_f32_16x16x32_bf16 v[32:35], v[158:161], v[174:177], v[32:35]
	v_mfma_f32_16x16x32_bf16 v[36:39], v[150:153], v[174:177], v[36:39]
	v_mfma_f32_16x16x32_bf16 v[20:23], v[150:153], v[182:185], v[20:23]
	v_mfma_f32_16x16x32_bf16 v[16:19], v[158:161], v[182:185], v[16:19]
	v_mfma_f32_16x16x32_bf16 v[0:3], v[158:161], v[194:197], v[0:3]
	v_mfma_f32_16x16x32_bf16 v[4:7], v[150:153], v[194:197], v[4:7]
	v_mfma_f32_16x16x32_bf16 v[52:55], v[154:157], v[170:173], v[52:55]
	v_mfma_f32_16x16x32_bf16 v[48:51], v[162:165], v[170:173], v[48:51]
	v_mfma_f32_16x16x32_bf16 v[32:35], v[162:165], v[178:181], v[32:35]
	v_mfma_f32_16x16x32_bf16 v[36:39], v[154:157], v[178:181], v[36:39]
	v_mfma_f32_16x16x32_bf16 v[20:23], v[154:157], v[190:193], v[20:23]
	v_mfma_f32_16x16x32_bf16 v[16:19], v[162:165], v[190:193], v[16:19]
	v_mfma_f32_16x16x32_bf16 v[0:3], v[162:165], v[198:201], v[0:3]
	v_mfma_f32_16x16x32_bf16 v[4:7], v[154:157], v[198:201], v[4:7]
	s_barrier
	s_setprio 0
	s_add_i32 s81, s81, 2
	s_add_u32 s56, s56, 0x100
	s_addc_u32 s57, s57, 0
	s_cbranch_vccz .LBB0_816
	s_and_b64 vcc, exec, s[42:43]
	s_cbranch_vccz .LBB0_819
	s_barrier

.LBB0_832:
	s_cmp_gt_u32 s90, 13
	s_cselect_b64 s[74:75], -1, 0
	s_and_b64 vcc, s[74:75], exec
	s_cselect_b32 s16, -14, 2
	s_add_i32 s74, s16, s90
	s_ashr_i32 s75, s74, 31
	s_lshl_b64 s[74:75], s[74:75], 7
	s_add_u32 s16, s42, s74
	s_addc_u32 s17, s43, s75
	s_add_u32 s50, s40, s74
	s_addc_u32 s76, s41, s75
	s_cmp_gt_u32 s90, 12
	s_cselect_b32 s74, -13, 3
	s_add_i32 s74, s74, s90
	s_ashr_i32 s75, s74, 31
	s_lshl_b64 s[74:75], s[74:75], 7
	s_add_u32 s77, s42, s74
	s_addc_u32 s91, s43, s75
	s_add_u32 s92, s40, s74
	s_addc_u32 s94, s41, s75
	s_cmp_eq_u32 s90, 14
	s_cselect_b32 s78, s58, s16
	s_mov_b32 s16, s90
	v_add_u32_e32 v108, 0x10000, v193
	v_add_u32_e32 v140, 0x14000, v193
	ds_read_b128 v[88:91], v108
	ds_read_b128 v[92:95], v108 offset:1024
	ds_read_b128 v[104:107], v108 offset:2048
	ds_read_b128 v[108:111], v108 offset:3072
	ds_read_b128 v[120:123], v140
	ds_read_b128 v[124:127], v140 offset:1024
	ds_read_b128 v[136:139], v140 offset:2048
	ds_read_b128 v[140:143], v140 offset:3072
	s_cselect_b32 s79, s59, s17
	s_cselect_b32 s81, s9, s76
	s_cselect_b32 s80, s10, s50
	s_cselect_b32 s75, s12, s91
	s_cselect_b32 s74, s11, s77
	s_cselect_b32 s77, s89, s94
	s_cselect_b32 s76, s27, s92
	ds_read_b128 v[152:155], v194
	ds_read_b128 v[156:159], v194 offset:1024
	ds_read_b128 v[168:171], v194 offset:2048
	ds_read_b128 v[172:175], v194 offset:3072
	ds_read_b128 v[176:179], v194 offset:4096
	ds_read_b128 v[180:183], v194 offset:5120
	ds_read_b128 v[184:187], v194 offset:6144
	ds_read_b128 v[196:199], v194 offset:7168
	s_add_u32 s16, s62, 0x220080
	s_addc_u32 s17, s63, 0
	s_mov_b32 m0, s82
	s_nop 0
	global_load_lds_dwordx4 v190, s[16:17]
	s_add_i32 s50, s19, 0xe000
	s_mov_b32 m0, s50
	s_nop 0
	global_load_lds_dwordx4 v192, s[16:17]
	s_setprio 1
	s_waitcnt vmcnt(8)
	s_waitcnt lgkmcnt(0)
	s_barrier
	v_mfma_f32_16x16x32_bf16 v[164:167], v[88:91], v[152:155], v[164:167]
	v_mfma_f32_16x16x32_bf16 v[160:163], v[104:107], v[152:155], v[160:163]
	v_mfma_f32_16x16x32_bf16 v[128:131], v[104:107], v[168:171], v[128:131]
	v_mfma_f32_16x16x32_bf16 v[132:135], v[88:91], v[168:171], v[132:135]
	v_mfma_f32_16x16x32_bf16 v[100:103], v[88:91], v[176:179], v[100:103]
	v_mfma_f32_16x16x32_bf16 v[96:99], v[104:107], v[176:179], v[96:99]
	v_mfma_f32_16x16x32_bf16 v[72:75], v[104:107], v[184:187], v[72:75]
	v_mfma_f32_16x16x32_bf16 v[76:79], v[88:91], v[184:187], v[76:79]
	v_mfma_f32_16x16x32_bf16 v[164:167], v[92:95], v[156:159], v[164:167]
	v_mfma_f32_16x16x32_bf16 v[160:163], v[108:111], v[156:159], v[160:163]
	v_mfma_f32_16x16x32_bf16 v[128:131], v[108:111], v[172:175], v[128:131]
	v_mfma_f32_16x16x32_bf16 v[132:135], v[92:95], v[172:175], v[132:135]
	v_mfma_f32_16x16x32_bf16 v[100:103], v[92:95], v[180:183], v[100:103]
	v_mfma_f32_16x16x32_bf16 v[96:99], v[108:111], v[180:183], v[96:99]
	v_mfma_f32_16x16x32_bf16 v[72:75], v[108:111], v[196:199], v[72:75]
	v_mfma_f32_16x16x32_bf16 v[76:79], v[92:95], v[196:199], v[76:79]
	v_mfma_f32_16x16x32_bf16 v[148:151], v[120:123], v[152:155], v[148:151]
	v_mfma_f32_16x16x32_bf16 v[144:147], v[136:139], v[152:155], v[144:147]
	v_mfma_f32_16x16x32_bf16 v[112:115], v[136:139], v[168:171], v[112:115]
	v_mfma_f32_16x16x32_bf16 v[116:119], v[120:123], v[168:171], v[116:119]
	v_mfma_f32_16x16x32_bf16 v[84:87], v[120:123], v[176:179], v[84:87]
	v_mfma_f32_16x16x32_bf16 v[80:83], v[136:139], v[176:179], v[80:83]
	v_mfma_f32_16x16x32_bf16 v[64:67], v[136:139], v[184:187], v[64:67]
	v_mfma_f32_16x16x32_bf16 v[68:71], v[120:123], v[184:187], v[68:71]
	v_mfma_f32_16x16x32_bf16 v[148:151], v[124:127], v[156:159], v[148:151]
	v_mfma_f32_16x16x32_bf16 v[144:147], v[140:143], v[156:159], v[144:147]
	v_mfma_f32_16x16x32_bf16 v[112:115], v[140:143], v[172:175], v[112:115]
	v_mfma_f32_16x16x32_bf16 v[116:119], v[124:127], v[172:175], v[116:119]
	v_mfma_f32_16x16x32_bf16 v[84:87], v[124:127], v[180:183], v[84:87]
	v_mfma_f32_16x16x32_bf16 v[80:83], v[140:143], v[180:183], v[80:83]
	v_mfma_f32_16x16x32_bf16 v[64:67], v[140:143], v[196:199], v[64:67]
	v_mfma_f32_16x16x32_bf16 v[68:71], v[124:127], v[196:199], v[68:71]
	s_barrier
	s_setprio 0
	ds_read_b128 v[152:155], v194 offset:16384
	ds_read_b128 v[156:159], v194 offset:17408
	ds_read_b128 v[168:171], v194 offset:18432
	ds_read_b128 v[172:175], v194 offset:19456
	ds_read_b128 v[176:179], v194 offset:20480
	ds_read_b128 v[180:183], v194 offset:21504
	ds_read_b128 v[184:187], v194 offset:22528
	ds_read_b128 v[196:199], v194 offset:23552
	s_mov_b32 m0, s28
	s_nop 0
	global_load_lds_dwordx4 v188, s[80:81]
	s_nop 0
	s_mov_b32 m0, s29
	s_nop 0
	global_load_lds_dwordx4 v191, s[80:81]
	s_add_u32 s16, s80, 0x40000
	s_addc_u32 s17, s81, 0
	s_mov_b32 m0, s34
	s_nop 0
	global_load_lds_dwordx4 v188, s[16:17]
	s_nop 0
	s_mov_b32 m0, s35
	s_nop 0
	global_load_lds_dwordx4 v191, s[16:17]
	s_mov_b32 m0, s19
	s_nop 0
	global_load_lds_dwordx4 v190, s[78:79]
	s_nop 0
	s_mov_b32 m0, s36
	s_nop 0
	global_load_lds_dwordx4 v192, s[78:79]
	s_setprio 1
	s_waitcnt vmcnt(8)
	s_waitcnt lgkmcnt(0)
	s_barrier
	v_mfma_f32_16x16x32_bf16 v[60:63], v[88:91], v[152:155], v[60:63]
	v_mfma_f32_16x16x32_bf16 v[56:59], v[104:107], v[152:155], v[56:59]
	v_mfma_f32_16x16x32_bf16 v[40:43], v[104:107], v[168:171], v[40:43]
	v_mfma_f32_16x16x32_bf16 v[44:47], v[88:91], v[168:171], v[44:47]
	v_mfma_f32_16x16x32_bf16 v[28:31], v[88:91], v[176:179], v[28:31]
	v_mfma_f32_16x16x32_bf16 v[24:27], v[104:107], v[176:179], v[24:27]
	v_mfma_f32_16x16x32_bf16 v[8:11], v[104:107], v[184:187], v[8:11]
	v_mfma_f32_16x16x32_bf16 v[12:15], v[88:91], v[184:187], v[12:15]
	v_mfma_f32_16x16x32_bf16 v[60:63], v[92:95], v[156:159], v[60:63]
	v_mfma_f32_16x16x32_bf16 v[56:59], v[108:111], v[156:159], v[56:59]
	v_mfma_f32_16x16x32_bf16 v[40:43], v[108:111], v[172:175], v[40:43]
	v_mfma_f32_16x16x32_bf16 v[44:47], v[92:95], v[172:175], v[44:47]
	v_mfma_f32_16x16x32_bf16 v[28:31], v[92:95], v[180:183], v[28:31]
	v_mfma_f32_16x16x32_bf16 v[24:27], v[108:111], v[180:183], v[24:27]
	v_mfma_f32_16x16x32_bf16 v[8:11], v[108:111], v[196:199], v[8:11]
	v_mfma_f32_16x16x32_bf16 v[12:15], v[92:95], v[196:199], v[12:15]
	v_mfma_f32_16x16x32_bf16 v[52:55], v[120:123], v[152:155], v[52:55]
	v_mfma_f32_16x16x32_bf16 v[48:51], v[136:139], v[152:155], v[48:51]
	v_mfma_f32_16x16x32_bf16 v[32:35], v[136:139], v[168:171], v[32:35]
	v_mfma_f32_16x16x32_bf16 v[36:39], v[120:123], v[168:171], v[36:39]
	v_mfma_f32_16x16x32_bf16 v[20:23], v[120:123], v[176:179], v[20:23]
	v_mfma_f32_16x16x32_bf16 v[16:19], v[136:139], v[176:179], v[16:19]
	v_mfma_f32_16x16x32_bf16 v[0:3], v[136:139], v[184:187], v[0:3]
	v_mfma_f32_16x16x32_bf16 v[4:7], v[120:123], v[184:187], v[4:7]
	v_mfma_f32_16x16x32_bf16 v[52:55], v[124:127], v[156:159], v[52:55]
	v_mfma_f32_16x16x32_bf16 v[48:51], v[140:143], v[156:159], v[48:51]
	v_mfma_f32_16x16x32_bf16 v[32:35], v[140:143], v[172:175], v[32:35]
	v_mfma_f32_16x16x32_bf16 v[36:39], v[124:127], v[172:175], v[36:39]
	v_mfma_f32_16x16x32_bf16 v[20:23], v[124:127], v[180:183], v[20:23]
	v_mfma_f32_16x16x32_bf16 v[16:19], v[140:143], v[180:183], v[16:19]
	v_mfma_f32_16x16x32_bf16 v[0:3], v[140:143], v[196:199], v[0:3]
	v_mfma_f32_16x16x32_bf16 v[4:7], v[124:127], v[196:199], v[4:7]
	s_barrier
	s_setprio 0
	v_add_u32_e32 v108, 0x18000, v193
	v_add_u32_e32 v140, 0x1c000, v193
	ds_read_b128 v[88:91], v108
	ds_read_b128 v[92:95], v108 offset:1024
	ds_read_b128 v[104:107], v108 offset:2048
	ds_read_b128 v[108:111], v108 offset:3072
	ds_read_b128 v[120:123], v140
	ds_read_b128 v[124:127], v140 offset:1024
	ds_read_b128 v[136:139], v140 offset:2048
	ds_read_b128 v[140:143], v140 offset:3072
	ds_read_b128 v[152:155], v194 offset:32768
	ds_read_b128 v[156:159], v194 offset:33792
	ds_read_b128 v[168:171], v194 offset:34816
	ds_read_b128 v[172:175], v194 offset:35840
	ds_read_b128 v[176:179], v194 offset:36864
	ds_read_b128 v[180:183], v194 offset:37888
	ds_read_b128 v[184:187], v194 offset:38912
	ds_read_b128 v[196:199], v194 offset:39936
	s_add_u32 s16, s78, 0x220000
	s_addc_u32 s17, s79, 0
	s_mov_b32 m0, s37
	s_nop 0
	global_load_lds_dwordx4 v190, s[16:17]
	s_nop 0
	s_mov_b32 m0, s65
	s_nop 0
	global_load_lds_dwordx4 v192, s[16:17]
	s_setprio 1
	s_waitcnt vmcnt(8)
	s_waitcnt lgkmcnt(0)
	s_barrier
	v_mfma_f32_16x16x32_bf16 v[164:167], v[88:91], v[152:155], v[164:167]
	v_mfma_f32_16x16x32_bf16 v[160:163], v[104:107], v[152:155], v[160:163]
	v_mfma_f32_16x16x32_bf16 v[128:131], v[104:107], v[168:171], v[128:131]
	v_mfma_f32_16x16x32_bf16 v[132:135], v[88:91], v[168:171], v[132:135]
	v_mfma_f32_16x16x32_bf16 v[100:103], v[88:91], v[176:179], v[100:103]
	v_mfma_f32_16x16x32_bf16 v[96:99], v[104:107], v[176:179], v[96:99]
	v_mfma_f32_16x16x32_bf16 v[72:75], v[104:107], v[184:187], v[72:75]
	v_mfma_f32_16x16x32_bf16 v[76:79], v[88:91], v[184:187], v[76:79]
	v_mfma_f32_16x16x32_bf16 v[164:167], v[92:95], v[156:159], v[164:167]
	v_mfma_f32_16x16x32_bf16 v[160:163], v[108:111], v[156:159], v[160:163]
	v_mfma_f32_16x16x32_bf16 v[128:131], v[108:111], v[172:175], v[128:131]
	v_mfma_f32_16x16x32_bf16 v[132:135], v[92:95], v[172:175], v[132:135]
	v_mfma_f32_16x16x32_bf16 v[100:103], v[92:95], v[180:183], v[100:103]
	v_mfma_f32_16x16x32_bf16 v[96:99], v[108:111], v[180:183], v[96:99]
	v_mfma_f32_16x16x32_bf16 v[72:75], v[108:111], v[196:199], v[72:75]
	v_mfma_f32_16x16x32_bf16 v[76:79], v[92:95], v[196:199], v[76:79]
	v_mfma_f32_16x16x32_bf16 v[148:151], v[120:123], v[152:155], v[148:151]
	v_mfma_f32_16x16x32_bf16 v[144:147], v[136:139], v[152:155], v[144:147]
	v_mfma_f32_16x16x32_bf16 v[112:115], v[136:139], v[168:171], v[112:115]
	v_mfma_f32_16x16x32_bf16 v[116:119], v[120:123], v[168:171], v[116:119]
	v_mfma_f32_16x16x32_bf16 v[84:87], v[120:123], v[176:179], v[84:87]
	v_mfma_f32_16x16x32_bf16 v[80:83], v[136:139], v[176:179], v[80:83]
	v_mfma_f32_16x16x32_bf16 v[64:67], v[136:139], v[184:187], v[64:67]
	v_mfma_f32_16x16x32_bf16 v[68:71], v[120:123], v[184:187], v[68:71]
	v_mfma_f32_16x16x32_bf16 v[148:151], v[124:127], v[156:159], v[148:151]
	v_mfma_f32_16x16x32_bf16 v[144:147], v[140:143], v[156:159], v[144:147]
	v_mfma_f32_16x16x32_bf16 v[112:115], v[140:143], v[172:175], v[112:115]
	v_mfma_f32_16x16x32_bf16 v[116:119], v[124:127], v[172:175], v[116:119]
	v_mfma_f32_16x16x32_bf16 v[84:87], v[124:127], v[180:183], v[84:87]
	v_mfma_f32_16x16x32_bf16 v[80:83], v[140:143], v[180:183], v[80:83]
	v_mfma_f32_16x16x32_bf16 v[64:67], v[140:143], v[196:199], v[64:67]
	v_mfma_f32_16x16x32_bf16 v[68:71], v[124:127], v[196:199], v[68:71]
	s_barrier
	s_setprio 0
	ds_read_b128 v[152:155], v194 offset:49152
	ds_read_b128 v[156:159], v194 offset:50176
	ds_read_b128 v[168:171], v194 offset:51200
	ds_read_b128 v[172:175], v194 offset:52224
	ds_read_b128 v[176:179], v194 offset:53248
	ds_read_b128 v[180:183], v194 offset:54272
	ds_read_b128 v[184:187], v194 offset:55296
	ds_read_b128 v[196:199], v194 offset:56320
	s_mov_b32 m0, s68
	s_nop 0
	global_load_lds_dwordx4 v188, s[76:77]
	s_nop 0
	s_mov_b32 m0, s30
	s_nop 0
	global_load_lds_dwordx4 v191, s[76:77]
	s_add_u32 s16, s76, 0x40000
	s_addc_u32 s17, s77, 0
	s_mov_b32 m0, s71
	s_nop 0
	global_load_lds_dwordx4 v188, s[16:17]
	s_nop 0
	s_mov_b32 m0, s72
	s_nop 0
	global_load_lds_dwordx4 v191, s[16:17]
	s_mov_b32 m0, s69
	s_nop 0
	global_load_lds_dwordx4 v190, s[74:75]
	s_nop 0
	s_mov_b32 m0, s70
	s_nop 0
	global_load_lds_dwordx4 v192, s[74:75]
	s_setprio 1
	s_waitcnt vmcnt(8)
	s_waitcnt lgkmcnt(0)
	s_barrier
	v_mfma_f32_16x16x32_bf16 v[60:63], v[88:91], v[152:155], v[60:63]
	v_mfma_f32_16x16x32_bf16 v[56:59], v[104:107], v[152:155], v[56:59]
	v_mfma_f32_16x16x32_bf16 v[40:43], v[104:107], v[168:171], v[40:43]
	v_mfma_f32_16x16x32_bf16 v[44:47], v[88:91], v[168:171], v[44:47]
	v_mfma_f32_16x16x32_bf16 v[28:31], v[88:91], v[176:179], v[28:31]
	v_mfma_f32_16x16x32_bf16 v[24:27], v[104:107], v[176:179], v[24:27]
	v_mfma_f32_16x16x32_bf16 v[8:11], v[104:107], v[184:187], v[8:11]
	v_mfma_f32_16x16x32_bf16 v[12:15], v[88:91], v[184:187], v[12:15]
	v_mfma_f32_16x16x32_bf16 v[60:63], v[92:95], v[156:159], v[60:63]
	v_mfma_f32_16x16x32_bf16 v[56:59], v[108:111], v[156:159], v[56:59]
	v_mfma_f32_16x16x32_bf16 v[40:43], v[108:111], v[172:175], v[40:43]
	v_mfma_f32_16x16x32_bf16 v[44:47], v[92:95], v[172:175], v[44:47]
	v_mfma_f32_16x16x32_bf16 v[28:31], v[92:95], v[180:183], v[28:31]
	v_mfma_f32_16x16x32_bf16 v[24:27], v[108:111], v[180:183], v[24:27]
	v_mfma_f32_16x16x32_bf16 v[8:11], v[108:111], v[196:199], v[8:11]
	v_mfma_f32_16x16x32_bf16 v[12:15], v[92:95], v[196:199], v[12:15]
	v_mfma_f32_16x16x32_bf16 v[52:55], v[120:123], v[152:155], v[52:55]
	v_mfma_f32_16x16x32_bf16 v[48:51], v[136:139], v[152:155], v[48:51]
	v_mfma_f32_16x16x32_bf16 v[32:35], v[136:139], v[168:171], v[32:35]
	v_mfma_f32_16x16x32_bf16 v[36:39], v[120:123], v[168:171], v[36:39]
	v_mfma_f32_16x16x32_bf16 v[20:23], v[120:123], v[176:179], v[20:23]
	v_mfma_f32_16x16x32_bf16 v[16:19], v[136:139], v[176:179], v[16:19]
	v_mfma_f32_16x16x32_bf16 v[0:3], v[136:139], v[184:187], v[0:3]
	v_mfma_f32_16x16x32_bf16 v[4:7], v[120:123], v[184:187], v[4:7]
	v_mfma_f32_16x16x32_bf16 v[52:55], v[124:127], v[156:159], v[52:55]
	v_mfma_f32_16x16x32_bf16 v[48:51], v[140:143], v[156:159], v[48:51]
	v_mfma_f32_16x16x32_bf16 v[32:35], v[140:143], v[172:175], v[32:35]
	v_mfma_f32_16x16x32_bf16 v[36:39], v[124:127], v[172:175], v[36:39]
	v_mfma_f32_16x16x32_bf16 v[20:23], v[124:127], v[180:183], v[20:23]
	v_mfma_f32_16x16x32_bf16 v[16:19], v[140:143], v[180:183], v[16:19]
	v_mfma_f32_16x16x32_bf16 v[0:3], v[140:143], v[196:199], v[0:3]
	v_mfma_f32_16x16x32_bf16 v[4:7], v[124:127], v[196:199], v[4:7]
	s_barrier
	s_setprio 0
	s_add_i32 s90, s90, 2
	s_add_u32 s62, s62, 0x100
	s_addc_u32 s63, s63, 0
	s_cbranch_vccz .LBB0_832
	s_and_b64 vcc, exec, s[54:55]
	s_cbranch_vccz .LBB0_835
	s_barrier

.LBB0_929:
	s_cmp_gt_u32 s66, 13
	s_cselect_b64 s[82:83], -1, 0
	s_and_b64 vcc, s[82:83], exec
	s_cselect_b32 s68, -14, 2
	s_add_i32 s82, s68, s66
	s_ashr_i32 s83, s82, 31
	s_lshl_b64 s[82:83], s[82:83], 7
	s_add_u32 s68, s76, s82
	s_addc_u32 s69, s77, s83
	s_add_u32 s84, s44, s82
	s_addc_u32 s85, s45, s83
	s_cmp_gt_u32 s66, 12
	s_cselect_b32 s82, -13, 3
	s_add_i32 s82, s82, s66
	s_ashr_i32 s83, s82, 31
	s_lshl_b64 s[82:83], s[82:83], 7
	s_add_u32 s37, s76, s82
	s_addc_u32 s13, s77, s83
	s_add_u32 s67, s44, s82
	s_addc_u32 s35, s45, s83
	s_cmp_eq_u32 s66, 14
	s_cselect_b32 s86, s27, s68
	s_mov_b32 s68, s66
	v_add_u32_e32 v140, 0x10000, v191
	v_add_u32_e32 v156, 0x14000, v191
	ds_read_b128 v[128:131], v140
	ds_read_b128 v[132:135], v140 offset:1024
	ds_read_b128 v[136:139], v140 offset:2048
	ds_read_b128 v[140:143], v140 offset:3072
	ds_read_b128 v[144:147], v156
	ds_read_b128 v[148:151], v156 offset:1024
	ds_read_b128 v[152:155], v156 offset:2048
	ds_read_b128 v[156:159], v156 offset:3072
	s_cselect_b32 s87, s1, s69
	s_cselect_b32 s89, s75, s85
	s_cselect_b32 s88, s9, s84
	s_cselect_b32 s83, s11, s13
	s_cselect_b32 s82, s10, s37
	s_cselect_b32 s85, s65, s35
	s_cselect_b32 s84, s12, s67
	ds_read_b128 v[160:163], v192
	ds_read_b128 v[164:167], v192 offset:1024
	ds_read_b128 v[168:171], v192 offset:2048
	ds_read_b128 v[172:175], v192 offset:3072
	ds_read_b128 v[176:179], v192 offset:4096
	ds_read_b128 v[180:183], v192 offset:5120
	ds_read_b128 v[194:197], v192 offset:6144
	ds_read_b128 v[198:201], v192 offset:7168
	s_add_u32 s68, s42, 0x40080
	s_addc_u32 s69, s43, 0
	s_mov_b32 m0, s31
	s_nop 0
	global_load_lds_dwordx4 v184, s[68:69]
	s_add_i32 s13, s2, 0xe000
	s_mov_b32 m0, s13
	s_nop 0
	global_load_lds_dwordx4 v186, s[68:69]
	s_setprio 1
	s_waitcnt vmcnt(8)
	s_waitcnt lgkmcnt(0)
	s_barrier
	v_mfma_i32_16x16x64_i8 v[124:127], v[128:131], v[160:163], v[124:127]
	v_mfma_i32_16x16x64_i8 v[120:123], v[136:139], v[160:163], v[120:123]
	v_mfma_i32_16x16x64_i8 v[112:115], v[136:139], v[168:171], v[112:115]
	v_mfma_i32_16x16x64_i8 v[116:119], v[128:131], v[168:171], v[116:119]
	v_mfma_i32_16x16x64_i8 v[108:111], v[128:131], v[176:179], v[108:111]
	v_mfma_i32_16x16x64_i8 v[104:107], v[136:139], v[176:179], v[104:107]
	v_mfma_i32_16x16x64_i8 v[96:99], v[136:139], v[194:197], v[96:99]
	v_mfma_i32_16x16x64_i8 v[100:103], v[128:131], v[194:197], v[100:103]
	v_mfma_i32_16x16x64_i8 v[124:127], v[132:135], v[164:167], v[124:127]
	v_mfma_i32_16x16x64_i8 v[120:123], v[140:143], v[164:167], v[120:123]
	v_mfma_i32_16x16x64_i8 v[112:115], v[140:143], v[172:175], v[112:115]
	v_mfma_i32_16x16x64_i8 v[116:119], v[132:135], v[172:175], v[116:119]
	v_mfma_i32_16x16x64_i8 v[108:111], v[132:135], v[180:183], v[108:111]
	v_mfma_i32_16x16x64_i8 v[104:107], v[140:143], v[180:183], v[104:107]
	v_mfma_i32_16x16x64_i8 v[96:99], v[140:143], v[198:201], v[96:99]
	v_mfma_i32_16x16x64_i8 v[100:103], v[132:135], v[198:201], v[100:103]
	v_mfma_i32_16x16x64_i8 v[92:95], v[144:147], v[160:163], v[92:95]
	v_mfma_i32_16x16x64_i8 v[88:91], v[152:155], v[160:163], v[88:91]
	v_mfma_i32_16x16x64_i8 v[80:83], v[152:155], v[168:171], v[80:83]
	v_mfma_i32_16x16x64_i8 v[84:87], v[144:147], v[168:171], v[84:87]
	v_mfma_i32_16x16x64_i8 v[76:79], v[144:147], v[176:179], v[76:79]
	v_mfma_i32_16x16x64_i8 v[72:75], v[152:155], v[176:179], v[72:75]
	v_mfma_i32_16x16x64_i8 v[64:67], v[152:155], v[194:197], v[64:67]
	v_mfma_i32_16x16x64_i8 v[68:71], v[144:147], v[194:197], v[68:71]
	v_mfma_i32_16x16x64_i8 v[92:95], v[148:151], v[164:167], v[92:95]
	v_mfma_i32_16x16x64_i8 v[88:91], v[156:159], v[164:167], v[88:91]
	v_mfma_i32_16x16x64_i8 v[80:83], v[156:159], v[172:175], v[80:83]
	v_mfma_i32_16x16x64_i8 v[84:87], v[148:151], v[172:175], v[84:87]
	v_mfma_i32_16x16x64_i8 v[76:79], v[148:151], v[180:183], v[76:79]
	v_mfma_i32_16x16x64_i8 v[72:75], v[156:159], v[180:183], v[72:75]
	v_mfma_i32_16x16x64_i8 v[64:67], v[156:159], v[198:201], v[64:67]
	v_mfma_i32_16x16x64_i8 v[68:71], v[148:151], v[198:201], v[68:71]
	s_barrier
	s_setprio 0
	ds_read_b128 v[160:163], v192 offset:16384
	ds_read_b128 v[164:167], v192 offset:17408
	ds_read_b128 v[168:171], v192 offset:18432
	ds_read_b128 v[172:175], v192 offset:19456
	ds_read_b128 v[176:179], v192 offset:20480
	ds_read_b128 v[180:183], v192 offset:21504
	ds_read_b128 v[194:197], v192 offset:22528
	ds_read_b128 v[198:201], v192 offset:23552
	s_mov_b32 m0, s3
	s_nop 0
	global_load_lds_dwordx4 v185, s[88:89]
	s_add_u32 s68, s88, 0x40000
	s_mov_b32 m0, s18
	s_nop 0
	global_load_lds_dwordx4 v187, s[88:89]
	s_addc_u32 s69, s89, 0
	s_mov_b32 m0, s19
	s_nop 0
	global_load_lds_dwordx4 v185, s[68:69]
	s_nop 0
	s_mov_b32 m0, s28
	s_nop 0
	global_load_lds_dwordx4 v187, s[68:69]
	s_nop 0
	s_mov_b32 m0, s2
	s_nop 0
	global_load_lds_dwordx4 v184, s[86:87]
	s_nop 0
	s_mov_b32 m0, s29
	s_nop 0
	global_load_lds_dwordx4 v186, s[86:87]
	s_setprio 1
	s_waitcnt vmcnt(8)
	s_waitcnt lgkmcnt(0)
	s_barrier
	v_mfma_i32_16x16x64_i8 v[60:63], v[128:131], v[160:163], v[60:63]
	v_mfma_i32_16x16x64_i8 v[56:59], v[136:139], v[160:163], v[56:59]
	v_mfma_i32_16x16x64_i8 v[48:51], v[136:139], v[168:171], v[48:51]
	v_mfma_i32_16x16x64_i8 v[52:55], v[128:131], v[168:171], v[52:55]
	v_mfma_i32_16x16x64_i8 v[44:47], v[128:131], v[176:179], v[44:47]
	v_mfma_i32_16x16x64_i8 v[40:43], v[136:139], v[176:179], v[40:43]
	v_mfma_i32_16x16x64_i8 v[32:35], v[136:139], v[194:197], v[32:35]
	v_mfma_i32_16x16x64_i8 v[36:39], v[128:131], v[194:197], v[36:39]
	v_mfma_i32_16x16x64_i8 v[60:63], v[132:135], v[164:167], v[60:63]
	v_mfma_i32_16x16x64_i8 v[56:59], v[140:143], v[164:167], v[56:59]
	v_mfma_i32_16x16x64_i8 v[48:51], v[140:143], v[172:175], v[48:51]
	v_mfma_i32_16x16x64_i8 v[52:55], v[132:135], v[172:175], v[52:55]
	v_mfma_i32_16x16x64_i8 v[44:47], v[132:135], v[180:183], v[44:47]
	v_mfma_i32_16x16x64_i8 v[40:43], v[140:143], v[180:183], v[40:43]
	v_mfma_i32_16x16x64_i8 v[32:35], v[140:143], v[198:201], v[32:35]
	v_mfma_i32_16x16x64_i8 v[36:39], v[132:135], v[198:201], v[36:39]
	v_mfma_i32_16x16x64_i8 v[28:31], v[144:147], v[160:163], v[28:31]
	v_mfma_i32_16x16x64_i8 v[24:27], v[152:155], v[160:163], v[24:27]
	v_mfma_i32_16x16x64_i8 v[16:19], v[152:155], v[168:171], v[16:19]
	v_mfma_i32_16x16x64_i8 v[20:23], v[144:147], v[168:171], v[20:23]
	v_mfma_i32_16x16x64_i8 v[12:15], v[144:147], v[176:179], v[12:15]
	v_mfma_i32_16x16x64_i8 v[8:11], v[152:155], v[176:179], v[8:11]
	v_mfma_i32_16x16x64_i8 v[0:3], v[152:155], v[194:197], v[0:3]
	v_mfma_i32_16x16x64_i8 v[4:7], v[144:147], v[194:197], v[4:7]
	v_mfma_i32_16x16x64_i8 v[28:31], v[148:151], v[164:167], v[28:31]
	v_mfma_i32_16x16x64_i8 v[24:27], v[156:159], v[164:167], v[24:27]
	v_mfma_i32_16x16x64_i8 v[16:19], v[156:159], v[172:175], v[16:19]
	v_mfma_i32_16x16x64_i8 v[20:23], v[148:151], v[172:175], v[20:23]
	v_mfma_i32_16x16x64_i8 v[12:15], v[148:151], v[180:183], v[12:15]
	v_mfma_i32_16x16x64_i8 v[8:11], v[156:159], v[180:183], v[8:11]
	v_mfma_i32_16x16x64_i8 v[0:3], v[156:159], v[198:201], v[0:3]
	v_mfma_i32_16x16x64_i8 v[4:7], v[148:151], v[198:201], v[4:7]
	s_barrier
	s_setprio 0
	v_add_u32_e32 v140, 0x18000, v191
	v_add_u32_e32 v156, 0x1c000, v191
	ds_read_b128 v[128:131], v140
	ds_read_b128 v[132:135], v140 offset:1024
	ds_read_b128 v[136:139], v140 offset:2048
	ds_read_b128 v[140:143], v140 offset:3072
	ds_read_b128 v[144:147], v156
	ds_read_b128 v[148:151], v156 offset:1024
	ds_read_b128 v[152:155], v156 offset:2048
	ds_read_b128 v[156:159], v156 offset:3072
	ds_read_b128 v[160:163], v192 offset:32768
	ds_read_b128 v[164:167], v192 offset:33792
	ds_read_b128 v[168:171], v192 offset:34816
	ds_read_b128 v[172:175], v192 offset:35840
	ds_read_b128 v[176:179], v192 offset:36864
	ds_read_b128 v[180:183], v192 offset:37888
	ds_read_b128 v[194:197], v192 offset:38912
	ds_read_b128 v[198:201], v192 offset:39936
	s_add_u32 s68, s86, 0x40000
	s_addc_u32 s69, s87, 0
	s_mov_b32 m0, s34
	s_nop 0
	global_load_lds_dwordx4 v184, s[68:69]
	s_nop 0
	s_mov_b32 m0, s36
	s_nop 0
	global_load_lds_dwordx4 v186, s[68:69]
	s_setprio 1
	s_waitcnt vmcnt(8)
	s_waitcnt lgkmcnt(0)
	s_barrier
	v_mfma_i32_16x16x64_i8 v[124:127], v[128:131], v[160:163], v[124:127]
	v_mfma_i32_16x16x64_i8 v[120:123], v[136:139], v[160:163], v[120:123]
	v_mfma_i32_16x16x64_i8 v[112:115], v[136:139], v[168:171], v[112:115]
	v_mfma_i32_16x16x64_i8 v[116:119], v[128:131], v[168:171], v[116:119]
	v_mfma_i32_16x16x64_i8 v[108:111], v[128:131], v[176:179], v[108:111]
	v_mfma_i32_16x16x64_i8 v[104:107], v[136:139], v[176:179], v[104:107]
	v_mfma_i32_16x16x64_i8 v[96:99], v[136:139], v[194:197], v[96:99]
	v_mfma_i32_16x16x64_i8 v[100:103], v[128:131], v[194:197], v[100:103]
	v_mfma_i32_16x16x64_i8 v[124:127], v[132:135], v[164:167], v[124:127]
	v_mfma_i32_16x16x64_i8 v[120:123], v[140:143], v[164:167], v[120:123]
	v_mfma_i32_16x16x64_i8 v[112:115], v[140:143], v[172:175], v[112:115]
	v_mfma_i32_16x16x64_i8 v[116:119], v[132:135], v[172:175], v[116:119]
	v_mfma_i32_16x16x64_i8 v[108:111], v[132:135], v[180:183], v[108:111]
	v_mfma_i32_16x16x64_i8 v[104:107], v[140:143], v[180:183], v[104:107]
	v_mfma_i32_16x16x64_i8 v[96:99], v[140:143], v[198:201], v[96:99]
	v_mfma_i32_16x16x64_i8 v[100:103], v[132:135], v[198:201], v[100:103]
	v_mfma_i32_16x16x64_i8 v[92:95], v[144:147], v[160:163], v[92:95]
	v_mfma_i32_16x16x64_i8 v[88:91], v[152:155], v[160:163], v[88:91]
	v_mfma_i32_16x16x64_i8 v[80:83], v[152:155], v[168:171], v[80:83]
	v_mfma_i32_16x16x64_i8 v[84:87], v[144:147], v[168:171], v[84:87]
	v_mfma_i32_16x16x64_i8 v[76:79], v[144:147], v[176:179], v[76:79]
	v_mfma_i32_16x16x64_i8 v[72:75], v[152:155], v[176:179], v[72:75]
	v_mfma_i32_16x16x64_i8 v[64:67], v[152:155], v[194:197], v[64:67]
	v_mfma_i32_16x16x64_i8 v[68:71], v[144:147], v[194:197], v[68:71]
	v_mfma_i32_16x16x64_i8 v[92:95], v[148:151], v[164:167], v[92:95]
	v_mfma_i32_16x16x64_i8 v[88:91], v[156:159], v[164:167], v[88:91]
	v_mfma_i32_16x16x64_i8 v[80:83], v[156:159], v[172:175], v[80:83]
	v_mfma_i32_16x16x64_i8 v[84:87], v[148:151], v[172:175], v[84:87]
	v_mfma_i32_16x16x64_i8 v[76:79], v[148:151], v[180:183], v[76:79]
	v_mfma_i32_16x16x64_i8 v[72:75], v[156:159], v[180:183], v[72:75]
	v_mfma_i32_16x16x64_i8 v[64:67], v[156:159], v[198:201], v[64:67]
	v_mfma_i32_16x16x64_i8 v[68:71], v[148:151], v[198:201], v[68:71]
	s_barrier
	s_setprio 0
	ds_read_b128 v[160:163], v192 offset:49152
	ds_read_b128 v[164:167], v192 offset:50176
	ds_read_b128 v[168:171], v192 offset:51200
	ds_read_b128 v[172:175], v192 offset:52224
	ds_read_b128 v[176:179], v192 offset:53248
	ds_read_b128 v[180:183], v192 offset:54272
	ds_read_b128 v[194:197], v192 offset:55296
	ds_read_b128 v[198:201], v192 offset:56320
	s_mov_b32 m0, s71
	s_nop 0
	global_load_lds_dwordx4 v185, s[84:85]
	s_add_u32 s68, s84, 0x40000
	s_mov_b32 m0, s72
	s_nop 0
	global_load_lds_dwordx4 v187, s[84:85]
	s_addc_u32 s69, s85, 0
	s_mov_b32 m0, s92
	s_nop 0
	global_load_lds_dwordx4 v185, s[68:69]
	s_nop 0
	s_mov_b32 m0, s94
	s_nop 0
	global_load_lds_dwordx4 v187, s[68:69]
	s_nop 0
	s_mov_b32 m0, s90
	s_nop 0
	global_load_lds_dwordx4 v184, s[82:83]
	s_nop 0
	s_mov_b32 m0, s91
	s_nop 0
	global_load_lds_dwordx4 v186, s[82:83]
	s_setprio 1
	s_waitcnt vmcnt(8)
	s_waitcnt lgkmcnt(0)
	s_barrier
	v_mfma_i32_16x16x64_i8 v[60:63], v[128:131], v[160:163], v[60:63]
	v_mfma_i32_16x16x64_i8 v[56:59], v[136:139], v[160:163], v[56:59]
	v_mfma_i32_16x16x64_i8 v[48:51], v[136:139], v[168:171], v[48:51]
	v_mfma_i32_16x16x64_i8 v[52:55], v[128:131], v[168:171], v[52:55]
	v_mfma_i32_16x16x64_i8 v[44:47], v[128:131], v[176:179], v[44:47]
	v_mfma_i32_16x16x64_i8 v[40:43], v[136:139], v[176:179], v[40:43]
	v_mfma_i32_16x16x64_i8 v[32:35], v[136:139], v[194:197], v[32:35]
	v_mfma_i32_16x16x64_i8 v[36:39], v[128:131], v[194:197], v[36:39]
	v_mfma_i32_16x16x64_i8 v[60:63], v[132:135], v[164:167], v[60:63]
	v_mfma_i32_16x16x64_i8 v[56:59], v[140:143], v[164:167], v[56:59]
	v_mfma_i32_16x16x64_i8 v[48:51], v[140:143], v[172:175], v[48:51]
	v_mfma_i32_16x16x64_i8 v[52:55], v[132:135], v[172:175], v[52:55]
	v_mfma_i32_16x16x64_i8 v[44:47], v[132:135], v[180:183], v[44:47]
	v_mfma_i32_16x16x64_i8 v[40:43], v[140:143], v[180:183], v[40:43]
	v_mfma_i32_16x16x64_i8 v[32:35], v[140:143], v[198:201], v[32:35]
	v_mfma_i32_16x16x64_i8 v[36:39], v[132:135], v[198:201], v[36:39]
	v_mfma_i32_16x16x64_i8 v[28:31], v[144:147], v[160:163], v[28:31]
	v_mfma_i32_16x16x64_i8 v[24:27], v[152:155], v[160:163], v[24:27]
	v_mfma_i32_16x16x64_i8 v[16:19], v[152:155], v[168:171], v[16:19]
	v_mfma_i32_16x16x64_i8 v[20:23], v[144:147], v[168:171], v[20:23]
	v_mfma_i32_16x16x64_i8 v[12:15], v[144:147], v[176:179], v[12:15]
	v_mfma_i32_16x16x64_i8 v[8:11], v[152:155], v[176:179], v[8:11]
	v_mfma_i32_16x16x64_i8 v[0:3], v[152:155], v[194:197], v[0:3]
	v_mfma_i32_16x16x64_i8 v[4:7], v[144:147], v[194:197], v[4:7]
	v_mfma_i32_16x16x64_i8 v[28:31], v[148:151], v[164:167], v[28:31]
	v_mfma_i32_16x16x64_i8 v[24:27], v[156:159], v[164:167], v[24:27]
	v_mfma_i32_16x16x64_i8 v[16:19], v[156:159], v[172:175], v[16:19]
	v_mfma_i32_16x16x64_i8 v[20:23], v[148:151], v[172:175], v[20:23]
	v_mfma_i32_16x16x64_i8 v[12:15], v[148:151], v[180:183], v[12:15]
	v_mfma_i32_16x16x64_i8 v[8:11], v[156:159], v[180:183], v[8:11]
	v_mfma_i32_16x16x64_i8 v[0:3], v[156:159], v[198:201], v[0:3]
	v_mfma_i32_16x16x64_i8 v[4:7], v[148:151], v[198:201], v[4:7]
	s_barrier
	s_setprio 0
	s_add_i32 s66, s66, 2
	s_add_u32 s42, s42, 0x100
	s_addc_u32 s43, s43, 0
	s_cbranch_vccz .LBB0_929
	s_and_b64 vcc, exec, s[50:51]
	s_cbranch_vccz .LBB0_932
	s_barrier

.LBB0_1309:
	s_cmp_gt_u32 s87, 13
	s_cselect_b64 s[60:61], -1, 0
	s_and_b64 vcc, s[60:61], exec
	s_cselect_b32 s60, -14, 2
	s_add_i32 s60, s60, s87
	s_ashr_i32 s61, s60, 31
	s_lshl_b64 s[60:61], s[60:61], 7
	s_add_u32 s62, s56, s60
	s_addc_u32 s63, s57, s61
	s_add_u32 s76, s54, s60
	s_addc_u32 s77, s55, s61
	s_cmp_gt_u32 s87, 12
	s_cselect_b32 s60, -13, 3
	s_add_i32 s60, s60, s87
	s_ashr_i32 s61, s60, 31
	s_lshl_b64 s[60:61], s[60:61], 7
	s_add_u32 s88, s56, s60
	s_addc_u32 s89, s57, s61
	s_add_u32 s90, s54, s60
	s_mov_b32 s60, s87
	v_add_u32_e32 v150, 0x10000, v136
	v_add_u32_e32 v166, 0x14000, v136
	ds_read_b128 v[138:141], v150
	ds_read_b128 v[142:145], v150 offset:1024
	ds_read_b128 v[146:149], v150 offset:2048
	ds_read_b128 v[150:153], v150 offset:3072
	ds_read_b128 v[154:157], v166
	ds_read_b128 v[158:161], v166 offset:1024
	ds_read_b128 v[162:165], v166 offset:2048
	ds_read_b128 v[166:169], v166 offset:3072
	s_addc_u32 s91, s55, s61
	s_cmp_eq_u32 s87, 14
	s_cselect_b32 s75, s43, s63
	s_cselect_b32 s74, s53, s62
	s_cselect_b32 s77, s47, s77
	s_cselect_b32 s76, s9, s76
	s_cselect_b32 s61, s11, s89
	s_cselect_b32 s60, s10, s88
	s_cselect_b32 s63, s86, s91
	s_cselect_b32 s62, s12, s90
	ds_read_b128 v[170:173], v137
	ds_read_b128 v[174:177], v137 offset:1024
	ds_read_b128 v[178:181], v137 offset:2048
	ds_read_b128 v[182:185], v137 offset:3072
	ds_read_b128 v[190:193], v137 offset:4096
	ds_read_b128 v[194:197], v137 offset:5120
	ds_read_b128 v[198:201], v137 offset:6144
	ds_read_b128 v[202:205], v137 offset:7168
	s_add_u32 s88, s58, 0x40080
	s_addc_u32 s89, s59, 0
	s_mov_b32 m0, s82
	s_nop 0
	global_load_lds_dwordx4 v132, s[88:89]
	s_add_i32 s90, s34, 0xe000
	s_mov_b32 m0, s90
	s_nop 0
	global_load_lds_dwordx4 v134, s[88:89]
	s_setprio 1
	s_waitcnt vmcnt(8)
	s_waitcnt lgkmcnt(0)
	s_barrier
	v_mfma_i32_16x16x64_i8 v[124:127], v[138:141], v[170:173], v[124:127]
	v_mfma_i32_16x16x64_i8 v[120:123], v[146:149], v[170:173], v[120:123]
	v_mfma_i32_16x16x64_i8 v[112:115], v[146:149], v[178:181], v[112:115]
	v_mfma_i32_16x16x64_i8 v[116:119], v[138:141], v[178:181], v[116:119]
	v_mfma_i32_16x16x64_i8 v[108:111], v[138:141], v[190:193], v[108:111]
	v_mfma_i32_16x16x64_i8 v[104:107], v[146:149], v[190:193], v[104:107]
	v_mfma_i32_16x16x64_i8 v[96:99], v[146:149], v[198:201], v[96:99]
	v_mfma_i32_16x16x64_i8 v[100:103], v[138:141], v[198:201], v[100:103]
	v_mfma_i32_16x16x64_i8 v[124:127], v[142:145], v[174:177], v[124:127]
	v_mfma_i32_16x16x64_i8 v[120:123], v[150:153], v[174:177], v[120:123]
	v_mfma_i32_16x16x64_i8 v[112:115], v[150:153], v[182:185], v[112:115]
	v_mfma_i32_16x16x64_i8 v[116:119], v[142:145], v[182:185], v[116:119]
	v_mfma_i32_16x16x64_i8 v[108:111], v[142:145], v[194:197], v[108:111]
	v_mfma_i32_16x16x64_i8 v[104:107], v[150:153], v[194:197], v[104:107]
	v_mfma_i32_16x16x64_i8 v[96:99], v[150:153], v[202:205], v[96:99]
	v_mfma_i32_16x16x64_i8 v[100:103], v[142:145], v[202:205], v[100:103]
	v_mfma_i32_16x16x64_i8 v[92:95], v[154:157], v[170:173], v[92:95]
	v_mfma_i32_16x16x64_i8 v[88:91], v[162:165], v[170:173], v[88:91]
	v_mfma_i32_16x16x64_i8 v[80:83], v[162:165], v[178:181], v[80:83]
	v_mfma_i32_16x16x64_i8 v[84:87], v[154:157], v[178:181], v[84:87]
	v_mfma_i32_16x16x64_i8 v[76:79], v[154:157], v[190:193], v[76:79]
	v_mfma_i32_16x16x64_i8 v[72:75], v[162:165], v[190:193], v[72:75]
	v_mfma_i32_16x16x64_i8 v[64:67], v[162:165], v[198:201], v[64:67]
	v_mfma_i32_16x16x64_i8 v[68:71], v[154:157], v[198:201], v[68:71]
	v_mfma_i32_16x16x64_i8 v[92:95], v[158:161], v[174:177], v[92:95]
	v_mfma_i32_16x16x64_i8 v[88:91], v[166:169], v[174:177], v[88:91]
	v_mfma_i32_16x16x64_i8 v[80:83], v[166:169], v[182:185], v[80:83]
	v_mfma_i32_16x16x64_i8 v[84:87], v[158:161], v[182:185], v[84:87]
	v_mfma_i32_16x16x64_i8 v[76:79], v[158:161], v[194:197], v[76:79]
	v_mfma_i32_16x16x64_i8 v[72:75], v[166:169], v[194:197], v[72:75]
	v_mfma_i32_16x16x64_i8 v[64:67], v[166:169], v[202:205], v[64:67]
	v_mfma_i32_16x16x64_i8 v[68:71], v[158:161], v[202:205], v[68:71]
	s_barrier
	s_setprio 0
	ds_read_b128 v[170:173], v137 offset:16384
	ds_read_b128 v[174:177], v137 offset:17408
	ds_read_b128 v[178:181], v137 offset:18432
	ds_read_b128 v[182:185], v137 offset:19456
	ds_read_b128 v[190:193], v137 offset:20480
	ds_read_b128 v[194:197], v137 offset:21504
	ds_read_b128 v[198:201], v137 offset:22528
	ds_read_b128 v[202:205], v137 offset:23552
	s_mov_b32 m0, s35
	s_nop 0
	global_load_lds_dwordx4 v133, s[76:77]
	s_nop 0
	s_mov_b32 m0, s36
	s_nop 0
	global_load_lds_dwordx4 v135, s[76:77]
	s_add_u32 s76, s76, 0x40000
	s_addc_u32 s77, s77, 0
	s_mov_b32 m0, s37
	s_nop 0
	global_load_lds_dwordx4 v133, s[76:77]
	s_nop 0
	s_mov_b32 m0, s65
	s_nop 0
	global_load_lds_dwordx4 v135, s[76:77]
	s_mov_b32 m0, s34
	s_nop 0
	global_load_lds_dwordx4 v132, s[74:75]
	s_nop 0
	s_mov_b32 m0, s66
	s_nop 0
	global_load_lds_dwordx4 v134, s[74:75]
	s_setprio 1
	s_waitcnt vmcnt(8)
	s_waitcnt lgkmcnt(0)
	s_barrier
	v_mfma_i32_16x16x64_i8 v[60:63], v[138:141], v[170:173], v[60:63]
	v_mfma_i32_16x16x64_i8 v[56:59], v[146:149], v[170:173], v[56:59]
	v_mfma_i32_16x16x64_i8 v[48:51], v[146:149], v[178:181], v[48:51]
	v_mfma_i32_16x16x64_i8 v[52:55], v[138:141], v[178:181], v[52:55]
	v_mfma_i32_16x16x64_i8 v[44:47], v[138:141], v[190:193], v[44:47]
	v_mfma_i32_16x16x64_i8 v[40:43], v[146:149], v[190:193], v[40:43]
	v_mfma_i32_16x16x64_i8 v[32:35], v[146:149], v[198:201], v[32:35]
	v_mfma_i32_16x16x64_i8 v[36:39], v[138:141], v[198:201], v[36:39]
	v_mfma_i32_16x16x64_i8 v[60:63], v[142:145], v[174:177], v[60:63]
	v_mfma_i32_16x16x64_i8 v[56:59], v[150:153], v[174:177], v[56:59]
	v_mfma_i32_16x16x64_i8 v[48:51], v[150:153], v[182:185], v[48:51]
	v_mfma_i32_16x16x64_i8 v[52:55], v[142:145], v[182:185], v[52:55]
	v_mfma_i32_16x16x64_i8 v[44:47], v[142:145], v[194:197], v[44:47]
	v_mfma_i32_16x16x64_i8 v[40:43], v[150:153], v[194:197], v[40:43]
	v_mfma_i32_16x16x64_i8 v[32:35], v[150:153], v[202:205], v[32:35]
	v_mfma_i32_16x16x64_i8 v[36:39], v[142:145], v[202:205], v[36:39]
	v_mfma_i32_16x16x64_i8 v[28:31], v[154:157], v[170:173], v[28:31]
	v_mfma_i32_16x16x64_i8 v[24:27], v[162:165], v[170:173], v[24:27]
	v_mfma_i32_16x16x64_i8 v[16:19], v[162:165], v[178:181], v[16:19]
	v_mfma_i32_16x16x64_i8 v[20:23], v[154:157], v[178:181], v[20:23]
	v_mfma_i32_16x16x64_i8 v[12:15], v[154:157], v[190:193], v[12:15]
	v_mfma_i32_16x16x64_i8 v[8:11], v[162:165], v[190:193], v[8:11]
	v_mfma_i32_16x16x64_i8 v[0:3], v[162:165], v[198:201], v[0:3]
	v_mfma_i32_16x16x64_i8 v[4:7], v[154:157], v[198:201], v[4:7]
	v_mfma_i32_16x16x64_i8 v[28:31], v[158:161], v[174:177], v[28:31]
	v_mfma_i32_16x16x64_i8 v[24:27], v[166:169], v[174:177], v[24:27]
	v_mfma_i32_16x16x64_i8 v[16:19], v[166:169], v[182:185], v[16:19]
	v_mfma_i32_16x16x64_i8 v[20:23], v[158:161], v[182:185], v[20:23]
	v_mfma_i32_16x16x64_i8 v[12:15], v[158:161], v[194:197], v[12:15]
	v_mfma_i32_16x16x64_i8 v[8:11], v[166:169], v[194:197], v[8:11]
	v_mfma_i32_16x16x64_i8 v[0:3], v[166:169], v[202:205], v[0:3]
	v_mfma_i32_16x16x64_i8 v[4:7], v[158:161], v[202:205], v[4:7]
	s_barrier
	s_setprio 0
	v_add_u32_e32 v150, 0x18000, v136
	v_add_u32_e32 v166, 0x1c000, v136
	ds_read_b128 v[138:141], v150
	ds_read_b128 v[142:145], v150 offset:1024
	ds_read_b128 v[146:149], v150 offset:2048
	ds_read_b128 v[150:153], v150 offset:3072
	ds_read_b128 v[154:157], v166
	ds_read_b128 v[158:161], v166 offset:1024
	ds_read_b128 v[162:165], v166 offset:2048
	ds_read_b128 v[166:169], v166 offset:3072
	ds_read_b128 v[170:173], v137 offset:32768
	ds_read_b128 v[174:177], v137 offset:33792
	ds_read_b128 v[178:181], v137 offset:34816
	ds_read_b128 v[182:185], v137 offset:35840
	ds_read_b128 v[190:193], v137 offset:36864
	ds_read_b128 v[194:197], v137 offset:37888
	ds_read_b128 v[198:201], v137 offset:38912
	ds_read_b128 v[202:205], v137 offset:39936
	s_add_u32 s74, s74, 0x40000
	s_addc_u32 s75, s75, 0
	s_mov_b32 m0, s67
	s_nop 0
	global_load_lds_dwordx4 v132, s[74:75]
	s_nop 0
	s_mov_b32 m0, s68
	s_nop 0
	global_load_lds_dwordx4 v134, s[74:75]
	s_setprio 1
	s_waitcnt vmcnt(8)
	s_waitcnt lgkmcnt(0)
	s_barrier
	v_mfma_i32_16x16x64_i8 v[124:127], v[138:141], v[170:173], v[124:127]
	v_mfma_i32_16x16x64_i8 v[120:123], v[146:149], v[170:173], v[120:123]
	v_mfma_i32_16x16x64_i8 v[112:115], v[146:149], v[178:181], v[112:115]
	v_mfma_i32_16x16x64_i8 v[116:119], v[138:141], v[178:181], v[116:119]
	v_mfma_i32_16x16x64_i8 v[108:111], v[138:141], v[190:193], v[108:111]
	v_mfma_i32_16x16x64_i8 v[104:107], v[146:149], v[190:193], v[104:107]
	v_mfma_i32_16x16x64_i8 v[96:99], v[146:149], v[198:201], v[96:99]
	v_mfma_i32_16x16x64_i8 v[100:103], v[138:141], v[198:201], v[100:103]
	v_mfma_i32_16x16x64_i8 v[124:127], v[142:145], v[174:177], v[124:127]
	v_mfma_i32_16x16x64_i8 v[120:123], v[150:153], v[174:177], v[120:123]
	v_mfma_i32_16x16x64_i8 v[112:115], v[150:153], v[182:185], v[112:115]
	v_mfma_i32_16x16x64_i8 v[116:119], v[142:145], v[182:185], v[116:119]
	v_mfma_i32_16x16x64_i8 v[108:111], v[142:145], v[194:197], v[108:111]
	v_mfma_i32_16x16x64_i8 v[104:107], v[150:153], v[194:197], v[104:107]
	v_mfma_i32_16x16x64_i8 v[96:99], v[150:153], v[202:205], v[96:99]
	v_mfma_i32_16x16x64_i8 v[100:103], v[142:145], v[202:205], v[100:103]
	v_mfma_i32_16x16x64_i8 v[92:95], v[154:157], v[170:173], v[92:95]
	v_mfma_i32_16x16x64_i8 v[88:91], v[162:165], v[170:173], v[88:91]
	v_mfma_i32_16x16x64_i8 v[80:83], v[162:165], v[178:181], v[80:83]
	v_mfma_i32_16x16x64_i8 v[84:87], v[154:157], v[178:181], v[84:87]
	v_mfma_i32_16x16x64_i8 v[76:79], v[154:157], v[190:193], v[76:79]
	v_mfma_i32_16x16x64_i8 v[72:75], v[162:165], v[190:193], v[72:75]
	v_mfma_i32_16x16x64_i8 v[64:67], v[162:165], v[198:201], v[64:67]
	v_mfma_i32_16x16x64_i8 v[68:71], v[154:157], v[198:201], v[68:71]
	v_mfma_i32_16x16x64_i8 v[92:95], v[158:161], v[174:177], v[92:95]
	v_mfma_i32_16x16x64_i8 v[88:91], v[166:169], v[174:177], v[88:91]
	v_mfma_i32_16x16x64_i8 v[80:83], v[166:169], v[182:185], v[80:83]
	v_mfma_i32_16x16x64_i8 v[84:87], v[158:161], v[182:185], v[84:87]
	v_mfma_i32_16x16x64_i8 v[76:79], v[158:161], v[194:197], v[76:79]
	v_mfma_i32_16x16x64_i8 v[72:75], v[166:169], v[194:197], v[72:75]
	v_mfma_i32_16x16x64_i8 v[64:67], v[166:169], v[202:205], v[64:67]
	v_mfma_i32_16x16x64_i8 v[68:71], v[158:161], v[202:205], v[68:71]
	s_barrier
	s_setprio 0
	ds_read_b128 v[170:173], v137 offset:49152
	ds_read_b128 v[174:177], v137 offset:50176
	ds_read_b128 v[178:181], v137 offset:51200
	ds_read_b128 v[182:185], v137 offset:52224
	ds_read_b128 v[190:193], v137 offset:53248
	ds_read_b128 v[194:197], v137 offset:54272
	ds_read_b128 v[198:201], v137 offset:55296
	ds_read_b128 v[202:205], v137 offset:56320
	s_mov_b32 m0, s71
	s_nop 0
	global_load_lds_dwordx4 v133, s[62:63]
	s_nop 0
	s_mov_b32 m0, s72
	s_nop 0
	global_load_lds_dwordx4 v135, s[62:63]
	s_add_u32 s62, s62, 0x40000
	s_addc_u32 s63, s63, 0
	s_mov_b32 m0, s80
	s_nop 0
	global_load_lds_dwordx4 v133, s[62:63]
	s_nop 0
	s_mov_b32 m0, s81
	s_nop 0
	global_load_lds_dwordx4 v135, s[62:63]
	s_mov_b32 m0, s78
	s_nop 0
	global_load_lds_dwordx4 v132, s[60:61]
	s_nop 0
	s_mov_b32 m0, s79
	s_nop 0
	global_load_lds_dwordx4 v134, s[60:61]
	s_setprio 1
	s_waitcnt vmcnt(8)
	s_waitcnt lgkmcnt(0)
	s_barrier
	v_mfma_i32_16x16x64_i8 v[60:63], v[138:141], v[170:173], v[60:63]
	v_mfma_i32_16x16x64_i8 v[56:59], v[146:149], v[170:173], v[56:59]
	v_mfma_i32_16x16x64_i8 v[48:51], v[146:149], v[178:181], v[48:51]
	v_mfma_i32_16x16x64_i8 v[52:55], v[138:141], v[178:181], v[52:55]
	v_mfma_i32_16x16x64_i8 v[44:47], v[138:141], v[190:193], v[44:47]
	v_mfma_i32_16x16x64_i8 v[40:43], v[146:149], v[190:193], v[40:43]
	v_mfma_i32_16x16x64_i8 v[32:35], v[146:149], v[198:201], v[32:35]
	v_mfma_i32_16x16x64_i8 v[36:39], v[138:141], v[198:201], v[36:39]
	v_mfma_i32_16x16x64_i8 v[60:63], v[142:145], v[174:177], v[60:63]
	v_mfma_i32_16x16x64_i8 v[56:59], v[150:153], v[174:177], v[56:59]
	v_mfma_i32_16x16x64_i8 v[48:51], v[150:153], v[182:185], v[48:51]
	v_mfma_i32_16x16x64_i8 v[52:55], v[142:145], v[182:185], v[52:55]
	v_mfma_i32_16x16x64_i8 v[44:47], v[142:145], v[194:197], v[44:47]
	v_mfma_i32_16x16x64_i8 v[40:43], v[150:153], v[194:197], v[40:43]
	v_mfma_i32_16x16x64_i8 v[32:35], v[150:153], v[202:205], v[32:35]
	v_mfma_i32_16x16x64_i8 v[36:39], v[142:145], v[202:205], v[36:39]
	v_mfma_i32_16x16x64_i8 v[28:31], v[154:157], v[170:173], v[28:31]
	v_mfma_i32_16x16x64_i8 v[24:27], v[162:165], v[170:173], v[24:27]
	v_mfma_i32_16x16x64_i8 v[16:19], v[162:165], v[178:181], v[16:19]
	v_mfma_i32_16x16x64_i8 v[20:23], v[154:157], v[178:181], v[20:23]
	v_mfma_i32_16x16x64_i8 v[12:15], v[154:157], v[190:193], v[12:15]
	v_mfma_i32_16x16x64_i8 v[8:11], v[162:165], v[190:193], v[8:11]
	v_mfma_i32_16x16x64_i8 v[0:3], v[162:165], v[198:201], v[0:3]
	v_mfma_i32_16x16x64_i8 v[4:7], v[154:157], v[198:201], v[4:7]
	v_mfma_i32_16x16x64_i8 v[28:31], v[158:161], v[174:177], v[28:31]
	v_mfma_i32_16x16x64_i8 v[24:27], v[166:169], v[174:177], v[24:27]
	v_mfma_i32_16x16x64_i8 v[16:19], v[166:169], v[182:185], v[16:19]
	v_mfma_i32_16x16x64_i8 v[20:23], v[158:161], v[182:185], v[20:23]
	v_mfma_i32_16x16x64_i8 v[12:15], v[158:161], v[194:197], v[12:15]
	v_mfma_i32_16x16x64_i8 v[8:11], v[166:169], v[194:197], v[8:11]
	v_mfma_i32_16x16x64_i8 v[0:3], v[166:169], v[202:205], v[0:3]
	v_mfma_i32_16x16x64_i8 v[4:7], v[158:161], v[202:205], v[4:7]
	s_barrier
	s_setprio 0
	s_add_i32 s87, s87, 2
	s_add_u32 s58, s58, 0x100
	s_addc_u32 s59, s59, 0
	s_cbranch_vccz .LBB0_1309
	s_and_b64 vcc, exec, s[40:41]
	s_cbranch_vccz .LBB0_1312
	s_barrier

.LBB0_1469:
	s_cmp_gt_u32 s76, 13
	s_cselect_b64 s[54:55], -1, 0
	s_and_b64 vcc, s[54:55], exec
	s_cselect_b32 s54, -14, 2
	s_add_i32 s54, s54, s76
	s_ashr_i32 s55, s54, 31
	s_lshl_b64 s[54:55], s[54:55], 7
	s_add_u32 s56, s50, s54
	s_addc_u32 s57, s51, s55
	s_add_u32 s60, s48, s54
	s_addc_u32 s61, s49, s55
	s_cmp_gt_u32 s76, 12
	s_cselect_b32 s54, -13, 3
	s_add_i32 s54, s54, s76
	s_ashr_i32 s55, s54, 31
	s_lshl_b64 s[54:55], s[54:55], 7
	s_add_u32 s77, s50, s54
	s_addc_u32 s78, s51, s55
	s_add_u32 s79, s48, s54
	s_mov_b32 s54, s76
	v_add_u32_e32 v150, 0x10000, v136
	v_add_u32_e32 v166, 0x14000, v136
	ds_read_b128 v[138:141], v150
	ds_read_b128 v[142:145], v150 offset:1024
	ds_read_b128 v[146:149], v150 offset:2048
	ds_read_b128 v[150:153], v150 offset:3072
	ds_read_b128 v[154:157], v166
	ds_read_b128 v[158:161], v166 offset:1024
	ds_read_b128 v[162:165], v166 offset:2048
	ds_read_b128 v[166:169], v166 offset:3072
	s_addc_u32 s80, s49, s55
	s_cmp_eq_u32 s76, 14
	s_cselect_b32 s59, s23, s57
	s_cselect_b32 s58, s74, s56
	s_cselect_b32 s61, s41, s61
	s_cselect_b32 s60, s9, s60
	s_cselect_b32 s55, s11, s78
	s_cselect_b32 s54, s10, s77
	s_cselect_b32 s57, s75, s80
	s_cselect_b32 s56, s12, s79
	ds_read_b128 v[170:173], v137
	ds_read_b128 v[174:177], v137 offset:1024
	ds_read_b128 v[178:181], v137 offset:2048
	ds_read_b128 v[182:185], v137 offset:3072
	ds_read_b128 v[190:193], v137 offset:4096
	ds_read_b128 v[194:197], v137 offset:5120
	ds_read_b128 v[198:201], v137 offset:6144
	ds_read_b128 v[202:205], v137 offset:7168
	s_add_u32 s78, s52, 0x40080
	s_addc_u32 s79, s53, 0
	s_mov_b32 m0, s69
	s_nop 0
	global_load_lds_dwordx4 v132, s[78:79]
	s_add_i32 s77, s19, 0xe000
	s_mov_b32 m0, s77
	s_nop 0
	global_load_lds_dwordx4 v134, s[78:79]
	s_setprio 1
	s_waitcnt vmcnt(8)
	s_waitcnt lgkmcnt(0)
	s_barrier
	v_mfma_i32_16x16x64_i8 v[124:127], v[138:141], v[170:173], v[124:127]
	v_mfma_i32_16x16x64_i8 v[120:123], v[146:149], v[170:173], v[120:123]
	v_mfma_i32_16x16x64_i8 v[112:115], v[146:149], v[178:181], v[112:115]
	v_mfma_i32_16x16x64_i8 v[116:119], v[138:141], v[178:181], v[116:119]
	v_mfma_i32_16x16x64_i8 v[108:111], v[138:141], v[190:193], v[108:111]
	v_mfma_i32_16x16x64_i8 v[104:107], v[146:149], v[190:193], v[104:107]
	v_mfma_i32_16x16x64_i8 v[96:99], v[146:149], v[198:201], v[96:99]
	v_mfma_i32_16x16x64_i8 v[100:103], v[138:141], v[198:201], v[100:103]
	v_mfma_i32_16x16x64_i8 v[124:127], v[142:145], v[174:177], v[124:127]
	v_mfma_i32_16x16x64_i8 v[120:123], v[150:153], v[174:177], v[120:123]
	v_mfma_i32_16x16x64_i8 v[112:115], v[150:153], v[182:185], v[112:115]
	v_mfma_i32_16x16x64_i8 v[116:119], v[142:145], v[182:185], v[116:119]
	v_mfma_i32_16x16x64_i8 v[108:111], v[142:145], v[194:197], v[108:111]
	v_mfma_i32_16x16x64_i8 v[104:107], v[150:153], v[194:197], v[104:107]
	v_mfma_i32_16x16x64_i8 v[96:99], v[150:153], v[202:205], v[96:99]
	v_mfma_i32_16x16x64_i8 v[100:103], v[142:145], v[202:205], v[100:103]
	v_mfma_i32_16x16x64_i8 v[92:95], v[154:157], v[170:173], v[92:95]
	v_mfma_i32_16x16x64_i8 v[88:91], v[162:165], v[170:173], v[88:91]
	v_mfma_i32_16x16x64_i8 v[80:83], v[162:165], v[178:181], v[80:83]
	v_mfma_i32_16x16x64_i8 v[84:87], v[154:157], v[178:181], v[84:87]
	v_mfma_i32_16x16x64_i8 v[76:79], v[154:157], v[190:193], v[76:79]
	v_mfma_i32_16x16x64_i8 v[72:75], v[162:165], v[190:193], v[72:75]
	v_mfma_i32_16x16x64_i8 v[64:67], v[162:165], v[198:201], v[64:67]
	v_mfma_i32_16x16x64_i8 v[68:71], v[154:157], v[198:201], v[68:71]
	v_mfma_i32_16x16x64_i8 v[92:95], v[158:161], v[174:177], v[92:95]
	v_mfma_i32_16x16x64_i8 v[88:91], v[166:169], v[174:177], v[88:91]
	v_mfma_i32_16x16x64_i8 v[80:83], v[166:169], v[182:185], v[80:83]
	v_mfma_i32_16x16x64_i8 v[84:87], v[158:161], v[182:185], v[84:87]
	v_mfma_i32_16x16x64_i8 v[76:79], v[158:161], v[194:197], v[76:79]
	v_mfma_i32_16x16x64_i8 v[72:75], v[166:169], v[194:197], v[72:75]
	v_mfma_i32_16x16x64_i8 v[64:67], v[166:169], v[202:205], v[64:67]
	v_mfma_i32_16x16x64_i8 v[68:71], v[158:161], v[202:205], v[68:71]
	s_barrier
	s_setprio 0
	ds_read_b128 v[170:173], v137 offset:16384
	ds_read_b128 v[174:177], v137 offset:17408
	ds_read_b128 v[178:181], v137 offset:18432
	ds_read_b128 v[182:185], v137 offset:19456
	ds_read_b128 v[190:193], v137 offset:20480
	ds_read_b128 v[194:197], v137 offset:21504
	ds_read_b128 v[198:201], v137 offset:22528
	ds_read_b128 v[202:205], v137 offset:23552
	s_mov_b32 m0, s27
	s_nop 0
	global_load_lds_dwordx4 v133, s[60:61]
	s_nop 0
	s_mov_b32 m0, s28
	s_nop 0
	global_load_lds_dwordx4 v135, s[60:61]
	s_add_u32 s60, s60, 0x40000
	s_addc_u32 s61, s61, 0
	s_mov_b32 m0, s29
	s_nop 0
	global_load_lds_dwordx4 v133, s[60:61]
	s_nop 0
	s_mov_b32 m0, s30
	s_nop 0
	global_load_lds_dwordx4 v135, s[60:61]
	s_mov_b32 m0, s19
	s_nop 0
	global_load_lds_dwordx4 v132, s[58:59]
	s_nop 0
	s_mov_b32 m0, s31
	s_nop 0
	global_load_lds_dwordx4 v134, s[58:59]
	s_setprio 1
	s_waitcnt vmcnt(8)
	s_waitcnt lgkmcnt(0)
	s_barrier
	v_mfma_i32_16x16x64_i8 v[60:63], v[138:141], v[170:173], v[60:63]
	v_mfma_i32_16x16x64_i8 v[56:59], v[146:149], v[170:173], v[56:59]
	v_mfma_i32_16x16x64_i8 v[48:51], v[146:149], v[178:181], v[48:51]
	v_mfma_i32_16x16x64_i8 v[52:55], v[138:141], v[178:181], v[52:55]
	v_mfma_i32_16x16x64_i8 v[44:47], v[138:141], v[190:193], v[44:47]
	v_mfma_i32_16x16x64_i8 v[40:43], v[146:149], v[190:193], v[40:43]
	v_mfma_i32_16x16x64_i8 v[32:35], v[146:149], v[198:201], v[32:35]
	v_mfma_i32_16x16x64_i8 v[36:39], v[138:141], v[198:201], v[36:39]
	v_mfma_i32_16x16x64_i8 v[60:63], v[142:145], v[174:177], v[60:63]
	v_mfma_i32_16x16x64_i8 v[56:59], v[150:153], v[174:177], v[56:59]
	v_mfma_i32_16x16x64_i8 v[48:51], v[150:153], v[182:185], v[48:51]
	v_mfma_i32_16x16x64_i8 v[52:55], v[142:145], v[182:185], v[52:55]
	v_mfma_i32_16x16x64_i8 v[44:47], v[142:145], v[194:197], v[44:47]
	v_mfma_i32_16x16x64_i8 v[40:43], v[150:153], v[194:197], v[40:43]
	v_mfma_i32_16x16x64_i8 v[32:35], v[150:153], v[202:205], v[32:35]
	v_mfma_i32_16x16x64_i8 v[36:39], v[142:145], v[202:205], v[36:39]
	v_mfma_i32_16x16x64_i8 v[28:31], v[154:157], v[170:173], v[28:31]
	v_mfma_i32_16x16x64_i8 v[24:27], v[162:165], v[170:173], v[24:27]
	v_mfma_i32_16x16x64_i8 v[16:19], v[162:165], v[178:181], v[16:19]
	v_mfma_i32_16x16x64_i8 v[20:23], v[154:157], v[178:181], v[20:23]
	v_mfma_i32_16x16x64_i8 v[12:15], v[154:157], v[190:193], v[12:15]
	v_mfma_i32_16x16x64_i8 v[8:11], v[162:165], v[190:193], v[8:11]
	v_mfma_i32_16x16x64_i8 v[0:3], v[162:165], v[198:201], v[0:3]
	v_mfma_i32_16x16x64_i8 v[4:7], v[154:157], v[198:201], v[4:7]
	v_mfma_i32_16x16x64_i8 v[28:31], v[158:161], v[174:177], v[28:31]
	v_mfma_i32_16x16x64_i8 v[24:27], v[166:169], v[174:177], v[24:27]
	v_mfma_i32_16x16x64_i8 v[16:19], v[166:169], v[182:185], v[16:19]
	v_mfma_i32_16x16x64_i8 v[20:23], v[158:161], v[182:185], v[20:23]
	v_mfma_i32_16x16x64_i8 v[12:15], v[158:161], v[194:197], v[12:15]
	v_mfma_i32_16x16x64_i8 v[8:11], v[166:169], v[194:197], v[8:11]
	v_mfma_i32_16x16x64_i8 v[0:3], v[166:169], v[202:205], v[0:3]
	v_mfma_i32_16x16x64_i8 v[4:7], v[158:161], v[202:205], v[4:7]
	s_barrier
	s_setprio 0
	v_add_u32_e32 v150, 0x18000, v136
	v_add_u32_e32 v166, 0x1c000, v136
	ds_read_b128 v[138:141], v150
	ds_read_b128 v[142:145], v150 offset:1024
	ds_read_b128 v[146:149], v150 offset:2048
	ds_read_b128 v[150:153], v150 offset:3072
	ds_read_b128 v[154:157], v166
	ds_read_b128 v[158:161], v166 offset:1024
	ds_read_b128 v[162:165], v166 offset:2048
	ds_read_b128 v[166:169], v166 offset:3072
	ds_read_b128 v[170:173], v137 offset:32768
	ds_read_b128 v[174:177], v137 offset:33792
	ds_read_b128 v[178:181], v137 offset:34816
	ds_read_b128 v[182:185], v137 offset:35840
	ds_read_b128 v[190:193], v137 offset:36864
	ds_read_b128 v[194:197], v137 offset:37888
	ds_read_b128 v[198:201], v137 offset:38912
	ds_read_b128 v[202:205], v137 offset:39936
	s_add_u32 s58, s58, 0x40000
	s_addc_u32 s59, s59, 0
	s_mov_b32 m0, s34
	s_nop 0
	global_load_lds_dwordx4 v132, s[58:59]
	s_nop 0
	s_mov_b32 m0, s35
	s_nop 0
	global_load_lds_dwordx4 v134, s[58:59]
	s_setprio 1
	s_waitcnt vmcnt(8)
	s_waitcnt lgkmcnt(0)
	s_barrier
	v_mfma_i32_16x16x64_i8 v[124:127], v[138:141], v[170:173], v[124:127]
	v_mfma_i32_16x16x64_i8 v[120:123], v[146:149], v[170:173], v[120:123]
	v_mfma_i32_16x16x64_i8 v[112:115], v[146:149], v[178:181], v[112:115]
	v_mfma_i32_16x16x64_i8 v[116:119], v[138:141], v[178:181], v[116:119]
	v_mfma_i32_16x16x64_i8 v[108:111], v[138:141], v[190:193], v[108:111]
	v_mfma_i32_16x16x64_i8 v[104:107], v[146:149], v[190:193], v[104:107]
	v_mfma_i32_16x16x64_i8 v[96:99], v[146:149], v[198:201], v[96:99]
	v_mfma_i32_16x16x64_i8 v[100:103], v[138:141], v[198:201], v[100:103]
	v_mfma_i32_16x16x64_i8 v[124:127], v[142:145], v[174:177], v[124:127]
	v_mfma_i32_16x16x64_i8 v[120:123], v[150:153], v[174:177], v[120:123]
	v_mfma_i32_16x16x64_i8 v[112:115], v[150:153], v[182:185], v[112:115]
	v_mfma_i32_16x16x64_i8 v[116:119], v[142:145], v[182:185], v[116:119]
	v_mfma_i32_16x16x64_i8 v[108:111], v[142:145], v[194:197], v[108:111]
	v_mfma_i32_16x16x64_i8 v[104:107], v[150:153], v[194:197], v[104:107]
	v_mfma_i32_16x16x64_i8 v[96:99], v[150:153], v[202:205], v[96:99]
	v_mfma_i32_16x16x64_i8 v[100:103], v[142:145], v[202:205], v[100:103]
	v_mfma_i32_16x16x64_i8 v[92:95], v[154:157], v[170:173], v[92:95]
	v_mfma_i32_16x16x64_i8 v[88:91], v[162:165], v[170:173], v[88:91]
	v_mfma_i32_16x16x64_i8 v[80:83], v[162:165], v[178:181], v[80:83]
	v_mfma_i32_16x16x64_i8 v[84:87], v[154:157], v[178:181], v[84:87]
	v_mfma_i32_16x16x64_i8 v[76:79], v[154:157], v[190:193], v[76:79]
	v_mfma_i32_16x16x64_i8 v[72:75], v[162:165], v[190:193], v[72:75]
	v_mfma_i32_16x16x64_i8 v[64:67], v[162:165], v[198:201], v[64:67]
	v_mfma_i32_16x16x64_i8 v[68:71], v[154:157], v[198:201], v[68:71]
	v_mfma_i32_16x16x64_i8 v[92:95], v[158:161], v[174:177], v[92:95]
	v_mfma_i32_16x16x64_i8 v[88:91], v[166:169], v[174:177], v[88:91]
	v_mfma_i32_16x16x64_i8 v[80:83], v[166:169], v[182:185], v[80:83]
	v_mfma_i32_16x16x64_i8 v[84:87], v[158:161], v[182:185], v[84:87]
	v_mfma_i32_16x16x64_i8 v[76:79], v[158:161], v[194:197], v[76:79]
	v_mfma_i32_16x16x64_i8 v[72:75], v[166:169], v[194:197], v[72:75]
	v_mfma_i32_16x16x64_i8 v[64:67], v[166:169], v[202:205], v[64:67]
	v_mfma_i32_16x16x64_i8 v[68:71], v[158:161], v[202:205], v[68:71]
	s_barrier
	s_setprio 0
	ds_read_b128 v[170:173], v137 offset:49152
	ds_read_b128 v[174:177], v137 offset:50176
	ds_read_b128 v[178:181], v137 offset:51200
	ds_read_b128 v[182:185], v137 offset:52224
	ds_read_b128 v[190:193], v137 offset:53248
	ds_read_b128 v[194:197], v137 offset:54272
	ds_read_b128 v[198:201], v137 offset:55296
	ds_read_b128 v[202:205], v137 offset:56320
	s_mov_b32 m0, s62
	s_nop 0
	global_load_lds_dwordx4 v133, s[56:57]
	s_nop 0
	s_mov_b32 m0, s63
	s_nop 0
	global_load_lds_dwordx4 v135, s[56:57]
	s_add_u32 s56, s56, 0x40000
	s_addc_u32 s57, s57, 0
	s_mov_b32 m0, s67
	s_nop 0
	global_load_lds_dwordx4 v133, s[56:57]
	s_nop 0
	s_mov_b32 m0, s68
	s_nop 0
	global_load_lds_dwordx4 v135, s[56:57]
	s_mov_b32 m0, s65
	s_nop 0
	global_load_lds_dwordx4 v132, s[54:55]
	s_nop 0
	s_mov_b32 m0, s66
	s_nop 0
	global_load_lds_dwordx4 v134, s[54:55]
	s_setprio 1
	s_waitcnt vmcnt(8)
	s_waitcnt lgkmcnt(0)
	s_barrier
	v_mfma_i32_16x16x64_i8 v[60:63], v[138:141], v[170:173], v[60:63]
	v_mfma_i32_16x16x64_i8 v[56:59], v[146:149], v[170:173], v[56:59]
	v_mfma_i32_16x16x64_i8 v[48:51], v[146:149], v[178:181], v[48:51]
	v_mfma_i32_16x16x64_i8 v[52:55], v[138:141], v[178:181], v[52:55]
	v_mfma_i32_16x16x64_i8 v[44:47], v[138:141], v[190:193], v[44:47]
	v_mfma_i32_16x16x64_i8 v[40:43], v[146:149], v[190:193], v[40:43]
	v_mfma_i32_16x16x64_i8 v[32:35], v[146:149], v[198:201], v[32:35]
	v_mfma_i32_16x16x64_i8 v[36:39], v[138:141], v[198:201], v[36:39]
	v_mfma_i32_16x16x64_i8 v[60:63], v[142:145], v[174:177], v[60:63]
	v_mfma_i32_16x16x64_i8 v[56:59], v[150:153], v[174:177], v[56:59]
	v_mfma_i32_16x16x64_i8 v[48:51], v[150:153], v[182:185], v[48:51]
	v_mfma_i32_16x16x64_i8 v[52:55], v[142:145], v[182:185], v[52:55]
	v_mfma_i32_16x16x64_i8 v[44:47], v[142:145], v[194:197], v[44:47]
	v_mfma_i32_16x16x64_i8 v[40:43], v[150:153], v[194:197], v[40:43]
	v_mfma_i32_16x16x64_i8 v[32:35], v[150:153], v[202:205], v[32:35]
	v_mfma_i32_16x16x64_i8 v[36:39], v[142:145], v[202:205], v[36:39]
	v_mfma_i32_16x16x64_i8 v[28:31], v[154:157], v[170:173], v[28:31]
	v_mfma_i32_16x16x64_i8 v[24:27], v[162:165], v[170:173], v[24:27]
	v_mfma_i32_16x16x64_i8 v[16:19], v[162:165], v[178:181], v[16:19]
	v_mfma_i32_16x16x64_i8 v[20:23], v[154:157], v[178:181], v[20:23]
	v_mfma_i32_16x16x64_i8 v[12:15], v[154:157], v[190:193], v[12:15]
	v_mfma_i32_16x16x64_i8 v[8:11], v[162:165], v[190:193], v[8:11]
	v_mfma_i32_16x16x64_i8 v[0:3], v[162:165], v[198:201], v[0:3]
	v_mfma_i32_16x16x64_i8 v[4:7], v[154:157], v[198:201], v[4:7]
	v_mfma_i32_16x16x64_i8 v[28:31], v[158:161], v[174:177], v[28:31]
	v_mfma_i32_16x16x64_i8 v[24:27], v[166:169], v[174:177], v[24:27]
	v_mfma_i32_16x16x64_i8 v[16:19], v[166:169], v[182:185], v[16:19]
	v_mfma_i32_16x16x64_i8 v[20:23], v[158:161], v[182:185], v[20:23]
	v_mfma_i32_16x16x64_i8 v[12:15], v[158:161], v[194:197], v[12:15]
	v_mfma_i32_16x16x64_i8 v[8:11], v[166:169], v[194:197], v[8:11]
	v_mfma_i32_16x16x64_i8 v[0:3], v[166:169], v[202:205], v[0:3]
	v_mfma_i32_16x16x64_i8 v[4:7], v[158:161], v[202:205], v[4:7]
	s_barrier
	s_setprio 0
	s_add_i32 s76, s76, 2
	s_add_u32 s52, s52, 0x100
	s_addc_u32 s53, s53, 0
	s_cbranch_vccz .LBB0_1469
	s_and_b64 vcc, exec, s[20:21]
	s_cbranch_vccz .LBB0_1472
	s_barrier
